# node0 tiles packed 4 per block so idle tail blocks exit immediately
# baseline (speedup 1.0000x reference)
_Z14k_bcount_node0ItEvPKiPiS2_PKfS4_S4_S4_PK15HIP_vector_typeIjLj4EEPtPT_SB_:
	s_cmpk_gt_u32 s2, 0xf4
	s_mov_b64 s[4:5], -1
	s_cbranch_scc0 .LBB5_8
	s_cmpk_ge_u32 s2, 0x403
	s_cbranch_scc1 .LBB5_84
	s_load_dwordx2 s[8:9], s[0:1], 0x20
	s_load_dwordx2 s[6:7], s[0:1], 0x38
	s_load_dwordx2 s[20:21], s[0:1], 0x18
	s_load_dword s22, s[0:1], 0x58
	v_mov_b32_e32 v3, 0
	v_lshlrev_b32_e32 v2, 4, v0
	v_cmp_gt_u32_e64 s[4:5], 16, v0
	s_waitcnt lgkmcnt(0)
	s_add_i32 s22, s22, 0xffffff0b
	s_add_i32 s23, s2, 0xffffff0b
	v_lshrrev_b32_e32 v150, 6, v0
	v_lshl_add_u32 v150, s23, 2, v150
	v_min_u32_e32 v150, 0xc34, v150
	v_and_b32_e32 v151, 31, v0
	v_lshl_or_b32 v150, v150, 5, v151
	v_mul_u32_u24_e32 v150, 0xc4, v150
	global_load_dwordx4 v[100:103], v150, s[20:21]
	global_load_dwordx4 v[104:107], v150, s[20:21] offset:16
	global_load_dwordx4 v[108:111], v150, s[20:21] offset:32
	global_load_dwordx4 v[112:115], v150, s[20:21] offset:48
	global_load_dwordx4 v[116:119], v150, s[20:21] offset:64
	global_load_dwordx4 v[120:123], v150, s[20:21] offset:80
	global_load_dwordx4 v[124:127], v150, s[20:21] offset:96
	global_load_dwordx4 v[128:131], v150, s[20:21] offset:112
	global_load_dwordx4 v[132:135], v150, s[20:21] offset:128
	global_load_dwordx4 v[136:139], v150, s[20:21] offset:144
	global_load_dwordx4 v[140:143], v150, s[20:21] offset:160
	global_load_dwordx4 v[144:147], v150, s[20:21] offset:176
	global_load_dword v148, v150, s[20:21] offset:192
	v_lshl_add_u64 v[4:5], s[8:9], 0, v[2:3]
	v_mov_b32_e32 v6, v3
	v_mov_b32_e32 v7, v3
	v_mov_b32_e32 v8, v3
	v_mov_b32_e32 v9, v3
	s_and_saveexec_b64 s[8:9], s[4:5]
	s_cbranch_execz .LBB5_3
	v_add_co_u32_e32 v6, vcc, 0x3000, v4
	s_nop 1
	v_addc_co_u32_e32 v7, vcc, 0, v5, vcc
	global_load_dwordx4 v[6:9], v[6:7], off
.LBB5_3:
	s_or_b64 exec, exec, s[8:9]
	v_lshl_add_u64 v[38:39], s[6:7], 0, v[2:3]
	v_add_co_u32_e32 v30, vcc, 0x1000, v38
	v_or_b32_e32 v1, 0x4000, v2
	s_nop 0
	v_addc_co_u32_e32 v31, vcc, 0, v39, vcc
	v_add_co_u32_e32 v32, vcc, 0x2000, v38
	global_load_dwordx4 v[10:13], v2, s[6:7]
	s_nop 0
	v_addc_co_u32_e32 v33, vcc, 0, v39, vcc
	v_add_co_u32_e32 v34, vcc, 0x3000, v38
	s_nop 1
	v_addc_co_u32_e32 v35, vcc, 0, v39, vcc
	v_add_co_u32_e32 v40, vcc, 0x5000, v38
	global_load_dwordx4 v[14:17], v[32:33], off
	global_load_dwordx4 v[18:21], v[34:35], off
	global_load_dwordx4 v[22:25], v[30:31], off
	global_load_dwordx4 v[26:29], v1, s[6:7]
	v_addc_co_u32_e32 v41, vcc, 0, v39, vcc
	v_add_co_u32_e32 v42, vcc, 0x6000, v38
	s_nop 1
	v_addc_co_u32_e32 v43, vcc, 0, v39, vcc
	v_add_co_u32_e32 v46, vcc, 0x7000, v38
	global_load_dwordx4 v[30:33], v[40:41], off
	global_load_dwordx4 v[34:37], v[42:43], off
	v_addc_co_u32_e32 v47, vcc, 0, v39, vcc
	v_add_co_u32_e32 v54, vcc, 0x1000, v4
	global_load_dwordx4 v[38:41], v[46:47], off
	global_load_dwordx4 v[42:45], v[4:5], off
	v_addc_co_u32_e32 v55, vcc, 0, v5, vcc
	v_add_co_u32_e32 v4, vcc, 0x2000, v4
	s_nop 1
	v_addc_co_u32_e32 v5, vcc, 0, v5, vcc
	global_load_dwordx4 v[46:49], v[54:55], off
	global_load_dwordx4 v[50:53], v[4:5], off
	s_load_dword s3, s[0:1], 0x58
	s_waitcnt vmcnt(10)
	ds_write_b128 v2, v[10:13]
	s_waitcnt vmcnt(7)
	ds_write_b128 v2, v[22:25] offset:4096
	s_waitcnt vmcnt(6)
	ds_write_b128 v2, v[26:29] offset:16384
	ds_write_b128 v2, v[14:17] offset:8192
	ds_write_b128 v2, v[18:21] offset:12288
	s_waitcnt vmcnt(5)
	ds_write_b128 v2, v[30:33] offset:20480
	s_waitcnt vmcnt(4)
	ds_write_b128 v2, v[34:37] offset:24576
	s_waitcnt vmcnt(3)
	ds_write_b128 v2, v[38:41] offset:28672
	s_waitcnt vmcnt(2)
	ds_write_b128 v2, v[42:45] offset:32768
	s_waitcnt vmcnt(1)
	ds_write_b128 v2, v[46:49] offset:36864
	s_waitcnt vmcnt(0)
	ds_write_b128 v2, v[50:53] offset:40960
	s_and_saveexec_b64 s[6:7], s[4:5]
	ds_write_b128 v2, v[6:9] offset:45056
	s_or_b64 exec, exec, s[6:7]
	s_waitcnt lgkmcnt(0)
	s_addk_i32 s3, 0xff0b
	v_lshrrev_b32_e32 v1, 6, v0
	s_add_i32 s4, s2, 0xffffff0b
	v_lshl_add_u32 v1, s4, 2, v1
	s_movk_i32 s3, 0xc35
	v_cmp_gt_i32_e32 vcc, s3, v1
	s_barrier
	s_and_saveexec_b64 s[8:9], vcc
	s_cbranch_execz .LBB5_7
	s_load_dwordx2 s[4:5], s[0:1], 0x18
	s_load_dwordx2 s[10:11], s[0:1], 0x50
	v_lshlrev_b32_e32 v69, 5, v1
	v_and_b32_e32 v1, 31, v0
	s_movk_i32 s3, 0xc4
	v_or_b32_e32 v66, v69, v1
	s_waitcnt lgkmcnt(0)
	v_mov_b64_e32 v[2:3], s[4:5]
	v_mad_i64_i32 v[50:51], s[4:5], v66, s3, v[2:3]
	s_waitcnt vmcnt(0)
	v_mov_b32_e32 v46, v100
	v_mov_b32_e32 v47, v101
	v_mov_b32_e32 v48, v102
	v_mov_b32_e32 v49, v103
	v_mov_b32_e32 v42, v104
	v_mov_b32_e32 v43, v105
	v_mov_b32_e32 v44, v106
	v_mov_b32_e32 v45, v107
	v_mov_b32_e32 v38, v108
	v_mov_b32_e32 v39, v109
	v_mov_b32_e32 v40, v110
	v_mov_b32_e32 v41, v111
	v_mov_b32_e32 v34, v112
	v_mov_b32_e32 v35, v113
	v_mov_b32_e32 v36, v114
	v_mov_b32_e32 v37, v115
	v_mov_b32_e32 v30, v116
	v_mov_b32_e32 v31, v117
	v_mov_b32_e32 v32, v118
	v_mov_b32_e32 v33, v119
	v_mov_b32_e32 v26, v120
	v_mov_b32_e32 v27, v121
	v_mov_b32_e32 v28, v122
	v_mov_b32_e32 v29, v123
	v_mov_b32_e32 v22, v124
	v_mov_b32_e32 v23, v125
	v_mov_b32_e32 v24, v126
	v_mov_b32_e32 v25, v127
	v_mov_b32_e32 v18, v128
	v_mov_b32_e32 v19, v129
	v_mov_b32_e32 v20, v130
	v_mov_b32_e32 v21, v131
	v_mov_b32_e32 v14, v132
	v_mov_b32_e32 v15, v133
	v_mov_b32_e32 v16, v134
	v_mov_b32_e32 v17, v135
	v_mov_b32_e32 v10, v136
	v_mov_b32_e32 v11, v137
	v_mov_b32_e32 v12, v138
	v_mov_b32_e32 v13, v139
	v_mov_b32_e32 v6, v140
	v_mov_b32_e32 v7, v141
	v_mov_b32_e32 v8, v142
	v_mov_b32_e32 v9, v143
	v_mov_b32_e32 v2, v144
	v_mov_b32_e32 v3, v145
	v_mov_b32_e32 v4, v146
	v_mov_b32_e32 v5, v147
	v_mov_b32_e32 v68, v148
	s_load_dwordx4 s[4:7], s[0:1], 0x28
	v_and_b32_e32 v71, 32, v0
	v_lshlrev_b32_e32 v50, 2, v71
	v_and_b32_e32 v72, 63, v0
	s_waitcnt vmcnt(5)
	v_mov_b32_e32 v70, v49
	s_waitcnt vmcnt(0)
	s_waitcnt lgkmcnt(0)
	global_load_dwordx4 v[58:61], v50, s[4:5] offset:112
	global_load_dwordx4 v[74:77], v50, s[4:5] offset:96
	global_load_dwordx4 v[78:81], v50, s[4:5] offset:80
	global_load_dwordx4 v[82:85], v50, s[4:5] offset:64
	global_load_dwordx4 v[86:89], v50, s[4:5]
	global_load_dwordx4 v[90:93], v50, s[4:5] offset:48
	global_load_dwordx4 v[94:97], v50, s[4:5] offset:16
	global_load_dwordx4 v[98:101], v50, s[4:5] offset:32
	v_lshlrev_b32_e32 v50, 2, v0
	v_and_b32_e32 v67, 0x80, v50
	ds_read_b128 v[102:105], v67 offset:32880
	ds_read_b128 v[106:109], v67 offset:32864
	ds_read_b128 v[110:113], v67 offset:33136
	ds_read_b128 v[114:117], v67 offset:33120
	ds_read_b128 v[118:121], v67 offset:33392
	ds_read_b128 v[122:125], v67 offset:33376
	ds_read_b128 v[126:129], v67 offset:32848
	ds_read_b128 v[130:133], v67 offset:32832
	ds_read_b128 v[134:137], v67 offset:33104
	ds_read_b128 v[138:141], v67 offset:33088
	ds_read_b128 v[142:145], v67 offset:33360
	ds_read_b128 v[146:149], v67 offset:33344
	ds_read_b128 v[62:65], v67 offset:33616
	ds_read_b128 v[50:53], v67 offset:33600
	ds_read_b128 v[54:57], v67 offset:33632
	s_waitcnt vmcnt(7) lgkmcnt(14)
	v_pk_fma_f32 v[104:105], v[46:47], v[104:105], v[60:61] op_sel_hi:[0,1,1]
	s_waitcnt vmcnt(6) lgkmcnt(13)
	v_pk_fma_f32 v[108:109], v[46:47], v[108:109], v[76:77] op_sel_hi:[0,1,1]
	v_pk_fma_f32 v[106:107], v[46:47], v[106:107], v[74:75] op_sel_hi:[0,1,1]
	ds_read_b128 v[74:77], v67 offset:32768
	s_waitcnt vmcnt(5) lgkmcnt(9)
	v_pk_fma_f32 v[128:129], v[46:47], v[128:129], v[80:81] op_sel_hi:[0,1,1]
	v_pk_fma_f32 v[126:127], v[46:47], v[126:127], v[78:79] op_sel_hi:[0,1,1]
	ds_read_b128 v[78:81], v67 offset:32816
	s_waitcnt vmcnt(4) lgkmcnt(9)
	v_pk_fma_f32 v[132:133], v[46:47], v[132:133], v[84:85] op_sel_hi:[0,1,1]
	v_pk_fma_f32 v[130:131], v[46:47], v[130:131], v[82:83] op_sel_hi:[0,1,1]
	ds_read_b128 v[82:85], v67 offset:32784
	s_waitcnt vmcnt(3) lgkmcnt(2)
	v_pk_fma_f32 v[150:151], v[46:47], v[74:75], v[86:87] op_sel_hi:[0,1,1]
	v_pk_fma_f32 v[152:153], v[46:47], v[76:77], v[88:89] op_sel_hi:[0,1,1]
	ds_read_b128 v[74:77], v67 offset:32800
	s_waitcnt vmcnt(2) lgkmcnt(2)
	v_pk_fma_f32 v[154:155], v[46:47], v[80:81], v[92:93] op_sel_hi:[0,1,1]
	v_pk_fma_f32 v[156:157], v[46:47], v[78:79], v[90:91] op_sel_hi:[0,1,1]
	ds_read_b128 v[78:81], v67 offset:33072
	s_waitcnt vmcnt(1) lgkmcnt(2)
	v_pk_fma_f32 v[158:159], v[46:47], v[82:83], v[94:95] op_sel_hi:[0,1,1]
	v_pk_fma_f32 v[160:161], v[46:47], v[84:85], v[96:97] op_sel_hi:[0,1,1]
	ds_read_b128 v[82:85], v67 offset:33024
	v_pk_fma_f32 v[102:103], v[46:47], v[102:103], v[58:59] op_sel_hi:[0,1,1]
	ds_read_b128 v[58:61], v67 offset:33648
	s_waitcnt vmcnt(0) lgkmcnt(3)
	v_pk_fma_f32 v[162:163], v[46:47], v[76:77], v[100:101] op_sel_hi:[0,1,1]
	v_pk_fma_f32 v[164:165], v[46:47], v[74:75], v[98:99] op_sel_hi:[0,1,1]
	ds_read_b128 v[74:77], v67 offset:33040
	ds_read_b128 v[86:89], v67 offset:33280
	ds_read_b128 v[90:93], v67 offset:33296
	v_pk_fma_f32 v[128:129], v[46:47], v[136:137], v[128:129] op_sel:[1,0,0]
	v_pk_fma_f32 v[126:127], v[46:47], v[134:135], v[126:127] op_sel:[1,0,0]
	s_waitcnt lgkmcnt(4)
	v_pk_fma_f32 v[134:135], v[46:47], v[82:83], v[150:151] op_sel:[1,0,0]
	v_pk_fma_f32 v[136:137], v[46:47], v[84:85], v[152:153] op_sel:[1,0,0]
	ds_read_b128 v[82:85], v67 offset:33056
	v_pk_fma_f32 v[112:113], v[46:47], v[112:113], v[104:105] op_sel:[1,0,0]
	v_pk_fma_f32 v[110:111], v[46:47], v[110:111], v[102:103] op_sel:[1,0,0]
	v_pk_fma_f32 v[116:117], v[46:47], v[116:117], v[108:109] op_sel:[1,0,0]
	v_pk_fma_f32 v[114:115], v[46:47], v[114:115], v[106:107] op_sel:[1,0,0]
	ds_read_b128 v[94:97], v67 offset:33536
	ds_read_b128 v[98:101], v67 offset:33552
	v_pk_fma_f32 v[132:133], v[46:47], v[140:141], v[132:133] op_sel:[1,0,0]
	v_pk_fma_f32 v[130:131], v[46:47], v[138:139], v[130:131] op_sel:[1,0,0]
	v_pk_fma_f32 v[138:139], v[46:47], v[80:81], v[154:155] op_sel:[1,0,0]
	v_pk_fma_f32 v[140:141], v[46:47], v[78:79], v[156:157] op_sel:[1,0,0]
	s_waitcnt lgkmcnt(5)
	v_pk_fma_f32 v[150:151], v[46:47], v[74:75], v[158:159] op_sel:[1,0,0]
	v_pk_fma_f32 v[152:153], v[46:47], v[76:77], v[160:161] op_sel:[1,0,0]
	ds_read_b128 v[74:77], v67 offset:33328
	s_waitcnt lgkmcnt(3)
	v_pk_fma_f32 v[154:155], v[46:47], v[84:85], v[162:163] op_sel:[1,0,0]
	v_pk_fma_f32 v[46:47], v[46:47], v[82:83], v[164:165] op_sel:[1,0,0]
	ds_read_b128 v[82:85], v67 offset:33312
	ds_read_b128 v[106:109], v67 offset:33584
	ds_read_b128 v[102:105], v67 offset:33792
	ds_read_b128 v[78:81], v67 offset:33808
	v_pk_fma_f32 v[156:157], v[48:49], v[120:121], v[112:113] op_sel_hi:[0,1,1]
	v_pk_fma_f32 v[158:159], v[48:49], v[118:119], v[110:111] op_sel_hi:[0,1,1]
	ds_read_b128 v[110:113], v67 offset:33568
	v_pk_fma_f32 v[128:129], v[48:49], v[144:145], v[128:129] op_sel_hi:[0,1,1]
	v_pk_fma_f32 v[126:127], v[48:49], v[142:143], v[126:127] op_sel_hi:[0,1,1]
	v_pk_fma_f32 v[124:125], v[48:49], v[124:125], v[116:117] op_sel_hi:[0,1,1]
	v_pk_fma_f32 v[122:123], v[48:49], v[122:123], v[114:115] op_sel_hi:[0,1,1]
	ds_read_b128 v[114:117], v67 offset:33824
	ds_read_b128 v[118:121], v67 offset:33840
	v_pk_fma_f32 v[134:135], v[48:49], v[86:87], v[134:135] op_sel_hi:[0,1,1]
	v_pk_fma_f32 v[136:137], v[48:49], v[88:89], v[136:137] op_sel_hi:[0,1,1]
	ds_read_b128 v[86:89], v67 offset:33856
	v_pk_fma_f32 v[142:143], v[48:49], v[90:91], v[150:151] op_sel_hi:[0,1,1]
	v_pk_fma_f32 v[144:145], v[48:49], v[92:93], v[152:153] op_sel_hi:[0,1,1]
	v_pk_fma_f32 v[150:151], v[70:71], v[62:63], v[126:127] op_sel_hi:[0,1,1]
	v_pk_fma_f32 v[152:153], v[70:71], v[64:65], v[128:129] op_sel_hi:[0,1,1]
	ds_read_b128 v[62:65], v67 offset:34048
	ds_read_b128 v[126:129], v67 offset:34304
	v_pk_fma_f32 v[130:131], v[48:49], v[146:147], v[130:131] op_sel_hi:[0,1,1]
	s_waitcnt lgkmcnt(10)
	v_pk_fma_f32 v[138:139], v[48:49], v[76:77], v[138:139] op_sel_hi:[0,1,1]
	v_pk_fma_f32 v[140:141], v[48:49], v[74:75], v[140:141] op_sel_hi:[0,1,1]
	s_waitcnt lgkmcnt(9)
	v_pk_fma_f32 v[146:147], v[48:49], v[84:85], v[154:155] op_sel_hi:[0,1,1]
	v_pk_fma_f32 v[154:155], v[70:71], v[58:59], v[158:159] op_sel_hi:[0,1,1]
	v_pk_fma_f32 v[156:157], v[70:71], v[60:61], v[156:157] op_sel_hi:[0,1,1]
	v_pk_fma_f32 v[58:59], v[70:71], v[94:95], v[134:135] op_sel_hi:[0,1,1]
	v_pk_fma_f32 v[60:61], v[70:71], v[96:97], v[136:137] op_sel_hi:[0,1,1]
	ds_read_b128 v[94:97], v67 offset:34560
	v_pk_fma_f32 v[132:133], v[48:49], v[148:149], v[132:133] op_sel_hi:[0,1,1]
	v_pk_fma_f32 v[148:149], v[48:49], v[82:83], v[46:47] op_sel_hi:[0,1,1]
	s_waitcnt lgkmcnt(9)
	v_pk_fma_f32 v[134:135], v[70:71], v[108:109], v[138:139] op_sel_hi:[0,1,1]
	v_pk_fma_f32 v[136:137], v[70:71], v[106:107], v[140:141] op_sel_hi:[0,1,1]
	v_pk_fma_f32 v[138:139], v[70:71], v[98:99], v[142:143] op_sel_hi:[0,1,1]
	v_pk_fma_f32 v[140:141], v[70:71], v[100:101], v[144:145] op_sel_hi:[0,1,1]
	ds_read_b128 v[98:101], v67 offset:34816
	v_pk_fma_f32 v[50:51], v[70:71], v[50:51], v[130:131] op_sel_hi:[0,1,1]
	s_waitcnt lgkmcnt(7)
	v_pk_fma_f32 v[142:143], v[70:71], v[112:113], v[146:147] op_sel_hi:[0,1,1]
	v_pk_fma_f32 v[144:145], v[70:71], v[110:111], v[148:149] op_sel_hi:[0,1,1]
	v_pk_fma_f32 v[146:147], v[42:43], v[102:103], v[58:59] op_sel_hi:[0,1,1]
	v_pk_fma_f32 v[148:149], v[42:43], v[104:105], v[60:61] op_sel_hi:[0,1,1]
	ds_read_b128 v[102:105], v67 offset:35072
	ds_read_b128 v[74:77], v67 offset:33872
	v_pk_fma_f32 v[54:55], v[70:71], v[54:55], v[122:123] op_sel_hi:[0,1,1]
	v_pk_fma_f32 v[56:57], v[70:71], v[56:57], v[124:125] op_sel_hi:[0,1,1]
	ds_read_b128 v[122:125], v67 offset:34064
	s_waitcnt lgkmcnt(9)
	v_pk_fma_f32 v[144:145], v[42:43], v[114:115], v[144:145] op_sel_hi:[0,1,1]
	v_pk_fma_f32 v[142:143], v[42:43], v[116:117], v[142:143] op_sel_hi:[0,1,1]
	ds_read_b128 v[114:117], v67 offset:35328
	s_waitcnt lgkmcnt(8)
	v_pk_fma_f32 v[158:159], v[42:43], v[86:87], v[50:51] op_sel_hi:[0,1,1]
	s_waitcnt lgkmcnt(7)
	v_pk_fma_f32 v[50:51], v[42:43], v[62:63], v[146:147] op_sel:[1,0,0]
	v_pk_fma_f32 v[62:63], v[42:43], v[64:65], v[148:149] op_sel:[1,0,0]
	v_mov_b32_e32 v48, v45
	v_pk_fma_f32 v[52:53], v[70:71], v[52:53], v[132:133] op_sel_hi:[0,1,1]
	ds_read_b128 v[130:133], v67 offset:34320
	s_waitcnt lgkmcnt(7)
	v_pk_fma_f32 v[62:63], v[44:45], v[128:129], v[62:63] op_sel_hi:[0,1,1]
	ds_read_b128 v[106:109], v67 offset:34576
	s_waitcnt lgkmcnt(7)
	v_pk_fma_f32 v[62:63], v[48:49], v[96:97], v[62:63] op_sel_hi:[0,1,1]
	ds_read_b128 v[110:113], v67 offset:34832
	s_waitcnt lgkmcnt(7)
	v_pk_fma_f32 v[62:63], v[38:39], v[100:101], v[62:63] op_sel_hi:[0,1,1]
	v_pk_fma_f32 v[138:139], v[42:43], v[78:79], v[138:139] op_sel_hi:[0,1,1]
	v_pk_fma_f32 v[140:141], v[42:43], v[80:81], v[140:141] op_sel_hi:[0,1,1]
	ds_read_b128 v[78:81], v67 offset:35088
	s_waitcnt lgkmcnt(7)
	v_pk_fma_f32 v[62:63], v[38:39], v[104:105], v[62:63] op_sel:[1,0,0]
	v_pk_fma_f32 v[136:137], v[42:43], v[118:119], v[136:137] op_sel_hi:[0,1,1]
	v_pk_fma_f32 v[134:135], v[42:43], v[120:121], v[134:135] op_sel_hi:[0,1,1]
	ds_read_b128 v[118:121], v67 offset:35344
	s_waitcnt lgkmcnt(5)
	v_pk_fma_f32 v[128:129], v[40:41], v[116:117], v[62:63] op_sel_hi:[0,1,1]
	v_pk_fma_f32 v[62:63], v[42:43], v[122:123], v[138:139] op_sel:[1,0,0]
	ds_read_b128 v[90:93], v67 offset:33888
	ds_read_b128 v[82:85], v67 offset:33904
	s_waitcnt lgkmcnt(6)
	v_pk_fma_f32 v[62:63], v[44:45], v[130:131], v[62:63] op_sel_hi:[0,1,1]
	s_waitcnt lgkmcnt(5)
	v_pk_fma_f32 v[62:63], v[48:49], v[106:107], v[62:63] op_sel_hi:[0,1,1]
	s_waitcnt lgkmcnt(4)
	v_pk_fma_f32 v[62:63], v[38:39], v[110:111], v[62:63] op_sel_hi:[0,1,1]
	s_waitcnt lgkmcnt(3)
	v_pk_fma_f32 v[62:63], v[38:39], v[78:79], v[62:63] op_sel:[1,0,0]
	v_pk_fma_f32 v[150:151], v[42:43], v[74:75], v[150:151] op_sel_hi:[0,1,1]
	s_waitcnt lgkmcnt(2)
	v_pk_fma_f32 v[118:119], v[40:41], v[118:119], v[62:63] op_sel_hi:[0,1,1]
	v_pk_fma_f32 v[62:63], v[42:43], v[124:125], v[140:141] op_sel:[1,0,0]
	v_pk_fma_f32 v[60:61], v[42:43], v[76:77], v[152:153] op_sel_hi:[0,1,1]
	v_pk_fma_f32 v[62:63], v[44:45], v[132:133], v[62:63] op_sel_hi:[0,1,1]
	v_pk_fma_f32 v[62:63], v[48:49], v[108:109], v[62:63] op_sel_hi:[0,1,1]
	v_pk_fma_f32 v[74:75], v[38:39], v[112:113], v[62:63] op_sel_hi:[0,1,1]
	ds_read_b128 v[62:65], v67 offset:34080
	v_pk_fma_f32 v[74:75], v[38:39], v[80:81], v[74:75] op_sel:[1,0,0]
	v_pk_fma_f32 v[160:161], v[42:43], v[88:89], v[52:53] op_sel_hi:[0,1,1]
	v_pk_fma_f32 v[120:121], v[40:41], v[120:121], v[74:75] op_sel_hi:[0,1,1]
	ds_read_b128 v[74:77], v67 offset:34336
	ds_read_b128 v[78:81], v67 offset:34096
	s_waitcnt lgkmcnt(4)
	v_pk_fma_f32 v[58:59], v[42:43], v[90:91], v[54:55] op_sel_hi:[0,1,1]
	s_waitcnt lgkmcnt(3)
	v_pk_fma_f32 v[54:55], v[42:43], v[82:83], v[154:155] op_sel_hi:[0,1,1]
	v_pk_fma_f32 v[52:53], v[42:43], v[84:85], v[156:157] op_sel_hi:[0,1,1]
	v_pk_fma_f32 v[50:51], v[44:45], v[126:127], v[50:51] op_sel_hi:[0,1,1]
	ds_read_b128 v[82:85], v67 offset:34592
	ds_read_b128 v[86:89], v67 offset:34352
	v_pk_fma_f32 v[56:57], v[42:43], v[92:93], v[56:57] op_sel_hi:[0,1,1]
	v_pk_fma_f32 v[50:51], v[48:49], v[94:95], v[50:51] op_sel_hi:[0,1,1]
	ds_read_b128 v[90:93], v67 offset:34848
	ds_read_b128 v[94:97], v67 offset:34608
	v_pk_fma_f32 v[50:51], v[38:39], v[98:99], v[50:51] op_sel_hi:[0,1,1]
	s_waitcnt lgkmcnt(6)
	v_pk_fma_f32 v[62:63], v[42:43], v[62:63], v[144:145] op_sel:[1,0,0]
	v_pk_fma_f32 v[50:51], v[38:39], v[102:103], v[50:51] op_sel:[1,0,0]
	s_waitcnt lgkmcnt(5)
	v_pk_fma_f32 v[62:63], v[44:45], v[74:75], v[62:63] op_sel_hi:[0,1,1]
	ds_read_b128 v[98:101], v67 offset:35104
	ds_read_b128 v[102:105], v67 offset:35360
	ds_read_b128 v[106:109], v67 offset:34864
	s_waitcnt lgkmcnt(6)
	v_pk_fma_f32 v[62:63], v[48:49], v[82:83], v[62:63] op_sel_hi:[0,1,1]
	s_waitcnt lgkmcnt(4)
	v_pk_fma_f32 v[62:63], v[38:39], v[90:91], v[62:63] op_sel_hi:[0,1,1]
	s_waitcnt lgkmcnt(2)
	v_pk_fma_f32 v[62:63], v[38:39], v[98:99], v[62:63] op_sel:[1,0,0]
	v_mov_b32_e32 v46, v41
	s_waitcnt lgkmcnt(1)
	v_pk_fma_f32 v[82:83], v[40:41], v[102:103], v[62:63] op_sel_hi:[0,1,1]
	v_pk_fma_f32 v[62:63], v[42:43], v[64:65], v[142:143] op_sel:[1,0,0]
	v_pk_fma_f32 v[126:127], v[40:41], v[114:115], v[50:51] op_sel_hi:[0,1,1]
	v_pk_fma_f32 v[62:63], v[44:45], v[76:77], v[62:63] op_sel_hi:[0,1,1]
	v_pk_fma_f32 v[74:75], v[48:49], v[84:85], v[62:63] op_sel_hi:[0,1,1]
	ds_read_b128 v[62:65], v67 offset:35584
	v_pk_fma_f32 v[84:85], v[38:39], v[92:93], v[74:75] op_sel_hi:[0,1,1]
	ds_read_b128 v[74:77], v67 offset:35600
	ds_read_b128 v[110:113], v67 offset:35120
	ds_read_b128 v[114:117], v67 offset:35376
	s_waitcnt lgkmcnt(3)
	v_pk_fma_f32 v[126:127], v[46:47], v[62:63], v[126:127] op_sel_hi:[0,1,1]
	v_pk_fma_f32 v[62:63], v[42:43], v[78:79], v[136:137] op_sel:[1,0,0]
	v_pk_fma_f32 v[128:129], v[46:47], v[64:65], v[128:129] op_sel_hi:[0,1,1]
	v_pk_fma_f32 v[62:63], v[44:45], v[86:87], v[62:63] op_sel_hi:[0,1,1]
	s_waitcnt lgkmcnt(2)
	v_pk_fma_f32 v[130:131], v[46:47], v[74:75], v[118:119] op_sel_hi:[0,1,1]
	v_pk_fma_f32 v[74:75], v[48:49], v[94:95], v[62:63] op_sel_hi:[0,1,1]
	ds_read_b128 v[62:65], v67 offset:35616
	v_pk_fma_f32 v[132:133], v[46:47], v[76:77], v[120:121] op_sel_hi:[0,1,1]
	v_pk_fma_f32 v[78:79], v[38:39], v[106:107], v[74:75] op_sel_hi:[0,1,1]
	ds_read_b128 v[74:77], v67 offset:35632
	v_pk_fma_f32 v[84:85], v[38:39], v[100:101], v[84:85] op_sel:[1,0,0]
	s_waitcnt lgkmcnt(1)
	v_pk_fma_f32 v[136:137], v[46:47], v[62:63], v[82:83] op_sel_hi:[0,1,1]
	v_pk_fma_f32 v[62:63], v[42:43], v[80:81], v[134:135] op_sel:[1,0,0]
	v_pk_fma_f32 v[78:79], v[38:39], v[110:111], v[78:79] op_sel:[1,0,0]
	v_pk_fma_f32 v[62:63], v[44:45], v[88:89], v[62:63] op_sel_hi:[0,1,1]
	v_pk_fma_f32 v[62:63], v[48:49], v[96:97], v[62:63] op_sel_hi:[0,1,1]
	v_pk_fma_f32 v[84:85], v[40:41], v[104:105], v[84:85] op_sel_hi:[0,1,1]
	v_pk_fma_f32 v[78:79], v[40:41], v[114:115], v[78:79] op_sel_hi:[0,1,1]
	v_pk_fma_f32 v[62:63], v[38:39], v[108:109], v[62:63] op_sel_hi:[0,1,1]
	v_pk_fma_f32 v[138:139], v[46:47], v[64:65], v[84:85] op_sel_hi:[0,1,1]
	s_waitcnt lgkmcnt(0)
	v_pk_fma_f32 v[140:141], v[46:47], v[74:75], v[78:79] op_sel_hi:[0,1,1]
	v_pk_fma_f32 v[74:75], v[38:39], v[112:113], v[62:63] op_sel:[1,0,0]
	ds_read_b128 v[62:65], v67 offset:34112
	v_pk_fma_f32 v[74:75], v[40:41], v[116:117], v[74:75] op_sel_hi:[0,1,1]
	v_pk_fma_f32 v[134:135], v[46:47], v[76:77], v[74:75] op_sel_hi:[0,1,1]
	ds_read_b128 v[74:77], v67 offset:34368
	ds_read_b128 v[78:81], v67 offset:34128
	ds_read_b128 v[82:85], v67 offset:34624
	ds_read_b128 v[86:89], v67 offset:34384
	ds_read_b128 v[90:93], v67 offset:34880
	ds_read_b128 v[94:97], v67 offset:34640
	s_waitcnt lgkmcnt(6)
	v_pk_fma_f32 v[62:63], v[42:43], v[62:63], v[158:159] op_sel:[1,0,0]
	ds_read_b128 v[98:101], v67 offset:35136
	ds_read_b128 v[102:105], v67 offset:34896
	s_waitcnt lgkmcnt(7)
	v_pk_fma_f32 v[62:63], v[44:45], v[74:75], v[62:63] op_sel_hi:[0,1,1]
	s_waitcnt lgkmcnt(5)
	v_pk_fma_f32 v[62:63], v[48:49], v[82:83], v[62:63] op_sel_hi:[0,1,1]
	ds_read_b128 v[106:109], v67 offset:35392
	ds_read_b128 v[110:113], v67 offset:35648
	ds_read_b128 v[114:117], v67 offset:35152
	s_waitcnt lgkmcnt(6)
	v_pk_fma_f32 v[62:63], v[38:39], v[90:91], v[62:63] op_sel_hi:[0,1,1]
	s_waitcnt lgkmcnt(4)
	v_pk_fma_f32 v[62:63], v[38:39], v[98:99], v[62:63] op_sel:[1,0,0]
	ds_read_b128 v[118:121], v67 offset:35408
	s_waitcnt lgkmcnt(3)
	v_pk_fma_f32 v[62:63], v[40:41], v[106:107], v[62:63] op_sel_hi:[0,1,1]
	s_waitcnt lgkmcnt(2)
	v_pk_fma_f32 v[90:91], v[46:47], v[110:111], v[62:63] op_sel_hi:[0,1,1]
	v_pk_fma_f32 v[62:63], v[42:43], v[64:65], v[160:161] op_sel:[1,0,0]
	v_pk_fma_f32 v[60:61], v[42:43], v[80:81], v[60:61] op_sel:[1,0,0]
	v_pk_fma_f32 v[62:63], v[44:45], v[76:77], v[62:63] op_sel_hi:[0,1,1]
	v_pk_fma_f32 v[62:63], v[48:49], v[84:85], v[62:63] op_sel_hi:[0,1,1]
	v_pk_fma_f32 v[74:75], v[38:39], v[92:93], v[62:63] op_sel_hi:[0,1,1]
	v_pk_fma_f32 v[74:75], v[38:39], v[100:101], v[74:75] op_sel:[1,0,0]
	ds_read_b128 v[62:65], v67 offset:35840
	v_pk_fma_f32 v[82:83], v[40:41], v[108:109], v[74:75] op_sel_hi:[0,1,1]
	ds_read_b128 v[74:77], v67 offset:35856
	v_pk_fma_f32 v[92:93], v[46:47], v[112:113], v[82:83] op_sel_hi:[0,1,1]
	ds_read_b128 v[82:85], v67 offset:35872
	s_waitcnt lgkmcnt(2)
	v_pk_fma_f32 v[126:127], v[34:35], v[62:63], v[126:127] op_sel_hi:[0,1,1]
	v_pk_fma_f32 v[128:129], v[34:35], v[64:65], v[128:129] op_sel_hi:[0,1,1]
	s_waitcnt lgkmcnt(1)
	v_pk_fma_f32 v[130:131], v[34:35], v[74:75], v[130:131] op_sel_hi:[0,1,1]
	v_pk_fma_f32 v[74:75], v[42:43], v[78:79], v[150:151] op_sel:[1,0,0]
	v_pk_fma_f32 v[132:133], v[34:35], v[76:77], v[132:133] op_sel_hi:[0,1,1]
	v_pk_fma_f32 v[74:75], v[44:45], v[86:87], v[74:75] op_sel_hi:[0,1,1]
	v_pk_fma_f32 v[74:75], v[48:49], v[94:95], v[74:75] op_sel_hi:[0,1,1]
	v_pk_fma_f32 v[74:75], v[38:39], v[102:103], v[74:75] op_sel_hi:[0,1,1]
	v_pk_fma_f32 v[74:75], v[38:39], v[114:115], v[74:75] op_sel:[1,0,0]
	ds_read_b128 v[62:65], v67 offset:35888
	v_pk_fma_f32 v[78:79], v[40:41], v[118:119], v[74:75] op_sel_hi:[0,1,1]
	ds_read_b128 v[74:77], v67 offset:35904
	ds_read_b128 v[122:125], v67 offset:35664
	v_pk_fma_f32 v[60:61], v[44:45], v[88:89], v[60:61] op_sel_hi:[0,1,1]
	s_waitcnt lgkmcnt(3)
	v_pk_fma_f32 v[136:137], v[34:35], v[82:83], v[136:137] op_sel_hi:[0,1,1]
	v_pk_fma_f32 v[138:139], v[34:35], v[84:85], v[138:139] op_sel_hi:[0,1,1]
	ds_read_b128 v[82:85], v67 offset:35920
	v_pk_fma_f32 v[60:61], v[48:49], v[96:97], v[60:61] op_sel_hi:[0,1,1]
	v_pk_fma_f32 v[60:61], v[38:39], v[104:105], v[60:61] op_sel_hi:[0,1,1]
	v_pk_fma_f32 v[60:61], v[38:39], v[116:117], v[60:61] op_sel:[1,0,0]
	s_waitcnt lgkmcnt(3)
	v_pk_fma_f32 v[140:141], v[34:35], v[62:63], v[140:141] op_sel_hi:[0,1,1]
	v_pk_fma_f32 v[64:65], v[34:35], v[64:65], v[134:135] op_sel_hi:[0,1,1]
	s_waitcnt lgkmcnt(2)
	v_pk_fma_f32 v[134:135], v[34:35], v[74:75], v[90:91] op_sel_hi:[0,1,1]
	v_pk_fma_f32 v[74:75], v[40:41], v[120:121], v[60:61] op_sel_hi:[0,1,1]
	ds_read_b128 v[60:63], v67 offset:34144
	s_waitcnt lgkmcnt(2)
	v_pk_fma_f32 v[78:79], v[46:47], v[122:123], v[78:79] op_sel_hi:[0,1,1]
	v_pk_fma_f32 v[74:75], v[46:47], v[124:125], v[74:75] op_sel_hi:[0,1,1]
	v_pk_fma_f32 v[142:143], v[34:35], v[76:77], v[92:93] op_sel_hi:[0,1,1]
	s_waitcnt lgkmcnt(1)
	v_pk_fma_f32 v[144:145], v[34:35], v[82:83], v[78:79] op_sel_hi:[0,1,1]
	v_pk_fma_f32 v[146:147], v[34:35], v[84:85], v[74:75] op_sel_hi:[0,1,1]
	ds_read_b128 v[74:77], v67 offset:34400
	ds_read_b128 v[78:81], v67 offset:34160
	s_waitcnt lgkmcnt(2)
	v_pk_fma_f32 v[86:87], v[42:43], v[60:61], v[58:59] op_sel:[1,0,0]
	ds_read_b128 v[58:61], v67 offset:34656
	ds_read_b128 v[82:85], v67 offset:34416
	v_pk_fma_f32 v[56:57], v[42:43], v[62:63], v[56:57] op_sel:[1,0,0]
	s_waitcnt lgkmcnt(3)
	v_pk_fma_f32 v[74:75], v[44:45], v[74:75], v[86:87] op_sel_hi:[0,1,1]
	ds_read_b128 v[86:89], v67 offset:34912
	ds_read_b128 v[90:93], v67 offset:34672
	ds_read_b128 v[94:97], v67 offset:35168
	ds_read_b128 v[98:101], v67 offset:34928
	ds_read_b128 v[102:105], v67 offset:35424
	ds_read_b128 v[106:109], v67 offset:35184
	ds_read_b128 v[110:113], v67 offset:36096
	ds_read_b128 v[114:117], v67 offset:35680
	ds_read_b128 v[118:121], v67 offset:35440
	s_waitcnt lgkmcnt(10)
	v_pk_fma_f32 v[58:59], v[48:49], v[58:59], v[74:75] op_sel_hi:[0,1,1]
	s_waitcnt lgkmcnt(8)
	v_pk_fma_f32 v[58:59], v[38:39], v[86:87], v[58:59] op_sel_hi:[0,1,1]
	ds_read_b128 v[122:125], v67 offset:36112
	s_waitcnt lgkmcnt(7)
	v_pk_fma_f32 v[58:59], v[38:39], v[94:95], v[58:59] op_sel:[1,0,0]
	s_waitcnt lgkmcnt(3)
	v_pk_fma_f32 v[86:87], v[34:35], v[110:111], v[126:127] op_sel:[1,0,0]
	v_pk_fma_f32 v[94:95], v[34:35], v[112:113], v[128:129] op_sel:[1,0,0]
	ds_read_b128 v[110:113], v67 offset:36128
	ds_read_b128 v[126:129], v67 offset:35696
	v_pk_fma_f32 v[58:59], v[40:41], v[102:103], v[58:59] op_sel_hi:[0,1,1]
	s_waitcnt lgkmcnt(2)
	v_pk_fma_f32 v[102:103], v[34:35], v[122:123], v[130:131] op_sel:[1,0,0]
	v_pk_fma_f32 v[130:131], v[34:35], v[124:125], v[132:133] op_sel:[1,0,0]
	ds_read_b128 v[122:125], v67 offset:36144
	s_waitcnt lgkmcnt(2)
	v_pk_fma_f32 v[132:133], v[34:35], v[110:111], v[136:137] op_sel:[1,0,0]
	v_pk_fma_f32 v[136:137], v[34:35], v[112:113], v[138:139] op_sel:[1,0,0]
	ds_read_b128 v[110:113], v67 offset:35936
	v_pk_fma_f32 v[56:57], v[44:45], v[76:77], v[56:57] op_sel_hi:[0,1,1]
	v_pk_fma_f32 v[56:57], v[48:49], v[60:61], v[56:57] op_sel_hi:[0,1,1]
	v_pk_fma_f32 v[56:57], v[38:39], v[88:89], v[56:57] op_sel_hi:[0,1,1]
	v_pk_fma_f32 v[60:61], v[38:39], v[96:97], v[56:57] op_sel:[1,0,0]
	v_pk_fma_f32 v[58:59], v[46:47], v[114:115], v[58:59] op_sel_hi:[0,1,1]
	v_pk_fma_f32 v[60:61], v[40:41], v[104:105], v[60:61] op_sel_hi:[0,1,1]
	v_pk_fma_f32 v[74:75], v[46:47], v[116:117], v[60:61] op_sel_hi:[0,1,1]
	ds_read_b128 v[60:63], v67 offset:36176
	s_waitcnt lgkmcnt(2)
	v_pk_fma_f32 v[114:115], v[34:35], v[122:123], v[140:141] op_sel:[1,0,0]
	v_pk_fma_f32 v[64:65], v[34:35], v[124:125], v[64:65] op_sel:[1,0,0]
	ds_read_b128 v[122:125], v67 offset:35952
	s_waitcnt lgkmcnt(2)
	v_pk_fma_f32 v[110:111], v[34:35], v[110:111], v[58:59] op_sel_hi:[0,1,1]
	ds_read_b128 v[56:59], v67 offset:36160
	v_pk_fma_f32 v[54:55], v[42:43], v[78:79], v[54:55] op_sel:[1,0,0]
	v_pk_fma_f32 v[42:43], v[42:43], v[80:81], v[52:53] op_sel:[1,0,0]
	v_pk_fma_f32 v[54:55], v[44:45], v[82:83], v[54:55] op_sel_hi:[0,1,1]
	v_pk_fma_f32 v[42:43], v[44:45], v[84:85], v[42:43] op_sel_hi:[0,1,1]
	v_pk_fma_f32 v[54:55], v[48:49], v[90:91], v[54:55] op_sel_hi:[0,1,1]
	v_pk_fma_f32 v[42:43], v[48:49], v[92:93], v[42:43] op_sel_hi:[0,1,1]
	v_pk_fma_f32 v[88:89], v[34:35], v[112:113], v[74:75] op_sel_hi:[0,1,1]
	ds_read_b128 v[74:77], v67 offset:36192
	s_waitcnt lgkmcnt(1)
	v_pk_fma_f32 v[96:97], v[34:35], v[56:57], v[134:135] op_sel:[1,0,0]
	v_pk_fma_f32 v[104:105], v[34:35], v[58:59], v[142:143] op_sel:[1,0,0]
	v_pk_fma_f32 v[112:113], v[34:35], v[60:61], v[144:145] op_sel:[1,0,0]
	v_pk_fma_f32 v[116:117], v[34:35], v[62:63], v[146:147] op_sel:[1,0,0]
	ds_read_b128 v[56:59], v67 offset:36208
	ds_read_b128 v[60:63], v67 offset:36352
	v_pk_fma_f32 v[54:55], v[38:39], v[98:99], v[54:55] op_sel_hi:[0,1,1]
	v_pk_fma_f32 v[42:43], v[38:39], v[100:101], v[42:43] op_sel_hi:[0,1,1]
	v_pk_fma_f32 v[54:55], v[38:39], v[106:107], v[54:55] op_sel:[1,0,0]
	v_pk_fma_f32 v[38:39], v[38:39], v[108:109], v[42:43] op_sel:[1,0,0]
	v_pk_fma_f32 v[54:55], v[40:41], v[118:119], v[54:55] op_sel_hi:[0,1,1]
	v_pk_fma_f32 v[38:39], v[40:41], v[120:121], v[38:39] op_sel_hi:[0,1,1]
	v_pk_fma_f32 v[54:55], v[46:47], v[126:127], v[54:55] op_sel_hi:[0,1,1]
	v_pk_fma_f32 v[42:43], v[46:47], v[128:129], v[38:39] op_sel_hi:[0,1,1]
	v_pk_fma_f32 v[54:55], v[34:35], v[122:123], v[54:55] op_sel_hi:[0,1,1]
	v_pk_fma_f32 v[42:43], v[34:35], v[124:125], v[42:43] op_sel_hi:[0,1,1]
	s_waitcnt lgkmcnt(2)
	v_pk_fma_f32 v[110:111], v[34:35], v[74:75], v[110:111] op_sel:[1,0,0]
	v_pk_fma_f32 v[88:89], v[34:35], v[76:77], v[88:89] op_sel:[1,0,0]
	s_waitcnt lgkmcnt(1)
	v_pk_fma_f32 v[78:79], v[34:35], v[56:57], v[54:55] op_sel:[1,0,0]
	s_waitcnt lgkmcnt(0)
	v_pk_fma_f32 v[82:83], v[36:37], v[60:61], v[86:87] op_sel_hi:[0,1,1]
	v_pk_fma_f32 v[86:87], v[36:37], v[62:63], v[94:95] op_sel_hi:[0,1,1]
	ds_read_b128 v[60:63], v67 offset:36400
	ds_read_b128 v[38:41], v67 offset:36416
	v_pk_fma_f32 v[34:35], v[34:35], v[58:59], v[42:43] op_sel:[1,0,0]
	ds_read_b128 v[42:45], v67 offset:36432
	ds_read_b128 v[46:49], v67 offset:36448
	ds_read_b128 v[54:57], v67 offset:36368
	ds_read_b128 v[74:77], v67 offset:36384
	s_waitcnt lgkmcnt(5)
	v_pk_fma_f32 v[62:63], v[36:37], v[62:63], v[64:65] op_sel_hi:[0,1,1]
	s_waitcnt lgkmcnt(4)
	v_pk_fma_f32 v[64:65], v[36:37], v[38:39], v[96:97] op_sel_hi:[0,1,1]
	v_pk_fma_f32 v[80:81], v[36:37], v[40:41], v[104:105] op_sel_hi:[0,1,1]
	s_waitcnt lgkmcnt(3)
	v_pk_fma_f32 v[84:85], v[36:37], v[42:43], v[112:113] op_sel_hi:[0,1,1]
	ds_read_b128 v[38:41], v67 offset:36464
	v_pk_fma_f32 v[90:91], v[36:37], v[44:45], v[116:117] op_sel_hi:[0,1,1]
	s_waitcnt lgkmcnt(3)
	v_pk_fma_f32 v[92:93], v[36:37], v[46:47], v[110:111] op_sel_hi:[0,1,1]
	ds_read_b128 v[42:45], v67 offset:36608
	v_pk_fma_f32 v[88:89], v[36:37], v[48:49], v[88:89] op_sel_hi:[0,1,1]
	ds_read_b128 v[46:49], v67 offset:36624
	v_mov_b32_e32 v50, v37
	s_waitcnt lgkmcnt(4)
	v_pk_fma_f32 v[54:55], v[36:37], v[54:55], v[102:103] op_sel_hi:[0,1,1]
	s_waitcnt lgkmcnt(2)
	v_pk_fma_f32 v[78:79], v[36:37], v[38:39], v[78:79] op_sel_hi:[0,1,1]
	v_pk_fma_f32 v[94:95], v[36:37], v[40:41], v[34:35] op_sel_hi:[0,1,1]
	s_waitcnt lgkmcnt(1)
	v_pk_fma_f32 v[34:35], v[50:51], v[42:43], v[82:83] op_sel_hi:[0,1,1]
	ds_read_b128 v[40:43], v67 offset:36640
	s_waitcnt lgkmcnt(1)
	v_pk_fma_f32 v[38:39], v[50:51], v[46:47], v[54:55] op_sel_hi:[0,1,1]
	ds_read_b128 v[52:55], v67 offset:36656
	v_pk_fma_f32 v[56:57], v[36:37], v[56:57], v[130:131] op_sel_hi:[0,1,1]
	v_pk_fma_f32 v[74:75], v[36:37], v[74:75], v[132:133] op_sel_hi:[0,1,1]
	v_pk_fma_f32 v[76:77], v[36:37], v[76:77], v[136:137] op_sel_hi:[0,1,1]
	v_pk_fma_f32 v[60:61], v[36:37], v[60:61], v[114:115] op_sel_hi:[0,1,1]
	v_pk_fma_f32 v[36:37], v[50:51], v[44:45], v[86:87] op_sel_hi:[0,1,1]
	v_pk_fma_f32 v[44:45], v[50:51], v[48:49], v[56:57] op_sel_hi:[0,1,1]
	ds_read_b128 v[56:59], v67 offset:36672
	s_waitcnt lgkmcnt(2)
	v_pk_fma_f32 v[46:47], v[50:51], v[40:41], v[74:75] op_sel_hi:[0,1,1]
	v_pk_fma_f32 v[48:49], v[50:51], v[42:43], v[76:77] op_sel_hi:[0,1,1]
	s_waitcnt lgkmcnt(1)
	v_pk_fma_f32 v[52:53], v[50:51], v[52:53], v[60:61] op_sel_hi:[0,1,1]
	v_pk_fma_f32 v[54:55], v[50:51], v[54:55], v[62:63] op_sel_hi:[0,1,1]
	ds_read_b128 v[40:43], v67 offset:36688
	ds_read_b128 v[60:63], v67 offset:36704
	s_waitcnt lgkmcnt(2)
	v_pk_fma_f32 v[110:111], v[50:51], v[56:57], v[64:65] op_sel_hi:[0,1,1]
	v_pk_fma_f32 v[112:113], v[50:51], v[58:59], v[80:81] op_sel_hi:[0,1,1]
	ds_read_b128 v[56:59], v67 offset:36720
	s_waitcnt lgkmcnt(2)
	v_pk_fma_f32 v[114:115], v[50:51], v[40:41], v[84:85] op_sel_hi:[0,1,1]
	s_waitcnt lgkmcnt(1)
	v_pk_fma_f32 v[118:119], v[50:51], v[60:61], v[92:93] op_sel_hi:[0,1,1]
	v_pk_fma_f32 v[120:121], v[50:51], v[62:63], v[88:89] op_sel_hi:[0,1,1]
	ds_read_b128 v[60:63], v67 offset:36976
	s_waitcnt lgkmcnt(1)
	v_pk_fma_f32 v[122:123], v[50:51], v[56:57], v[78:79] op_sel_hi:[0,1,1]
	v_pk_fma_f32 v[40:41], v[50:51], v[58:59], v[94:95] op_sel_hi:[0,1,1]
	ds_read_b128 v[56:59], v67 offset:37232
	ds_read_b128 v[74:77], v67 offset:37488
	ds_read_b128 v[78:81], v67 offset:36960
	ds_read_b128 v[86:89], v67 offset:37744
	s_waitcnt lgkmcnt(4)
	v_pk_fma_f32 v[40:41], v[30:31], v[62:63], v[40:41] op_sel_hi:[0,1,1]
	s_waitcnt lgkmcnt(3)
	v_pk_fma_f32 v[40:41], v[30:31], v[58:59], v[40:41] op_sel:[1,0,0]
	v_pk_fma_f32 v[58:59], v[30:31], v[60:61], v[122:123] op_sel_hi:[0,1,1]
	v_pk_fma_f32 v[116:117], v[50:51], v[42:43], v[90:91] op_sel_hi:[0,1,1]
	ds_read_b128 v[62:65], v67 offset:37216
	ds_read_b128 v[82:85], v67 offset:37472
	ds_read_b128 v[90:93], v67 offset:38000
	ds_read_b128 v[94:97], v67 offset:38256
	ds_read_b128 v[98:101], v67 offset:37728
	v_pk_fma_f32 v[56:57], v[30:31], v[56:57], v[58:59] op_sel:[1,0,0]
	s_waitcnt lgkmcnt(7)
	v_pk_fma_f32 v[42:43], v[32:33], v[76:77], v[40:41] op_sel_hi:[0,1,1]
	v_mov_b32_e32 v40, v33
	v_pk_fma_f32 v[56:57], v[32:33], v[74:75], v[56:57] op_sel_hi:[0,1,1]
	s_waitcnt lgkmcnt(5)
	v_pk_fma_f32 v[56:57], v[40:41], v[86:87], v[56:57] op_sel_hi:[0,1,1]
	ds_read_b128 v[102:105], v67 offset:37984
	ds_read_b128 v[106:109], v67 offset:38240
	s_waitcnt lgkmcnt(4)
	v_pk_fma_f32 v[56:57], v[26:27], v[90:91], v[56:57] op_sel_hi:[0,1,1]
	s_waitcnt lgkmcnt(3)
	v_pk_fma_f32 v[122:123], v[26:27], v[94:95], v[56:57] op_sel:[1,0,0]
	v_pk_fma_f32 v[56:57], v[30:31], v[80:81], v[120:121] op_sel_hi:[0,1,1]
	v_pk_fma_f32 v[56:57], v[30:31], v[64:65], v[56:57] op_sel:[1,0,0]
	v_pk_fma_f32 v[42:43], v[40:41], v[88:89], v[42:43] op_sel_hi:[0,1,1]
	v_pk_fma_f32 v[56:57], v[32:33], v[84:85], v[56:57] op_sel_hi:[0,1,1]
	s_waitcnt lgkmcnt(2)
	v_pk_fma_f32 v[56:57], v[40:41], v[100:101], v[56:57] op_sel_hi:[0,1,1]
	s_waitcnt lgkmcnt(1)
	v_pk_fma_f32 v[56:57], v[26:27], v[104:105], v[56:57] op_sel_hi:[0,1,1]
	s_waitcnt lgkmcnt(0)
	v_pk_fma_f32 v[120:121], v[26:27], v[108:109], v[56:57] op_sel:[1,0,0]
	v_pk_fma_f32 v[56:57], v[30:31], v[78:79], v[118:119] op_sel_hi:[0,1,1]
	v_pk_fma_f32 v[56:57], v[30:31], v[62:63], v[56:57] op_sel:[1,0,0]
	v_pk_fma_f32 v[42:43], v[26:27], v[92:93], v[42:43] op_sel_hi:[0,1,1]
	v_pk_fma_f32 v[56:57], v[32:33], v[82:83], v[56:57] op_sel_hi:[0,1,1]
	v_pk_fma_f32 v[60:61], v[40:41], v[98:99], v[56:57] op_sel_hi:[0,1,1]
	ds_read_b128 v[56:59], v67 offset:36944
	v_pk_fma_f32 v[60:61], v[26:27], v[102:103], v[60:61] op_sel_hi:[0,1,1]
	v_pk_fma_f32 v[118:119], v[26:27], v[106:107], v[60:61] op_sel:[1,0,0]
	ds_read_b128 v[60:63], v67 offset:37200
	ds_read_b128 v[74:77], v67 offset:36928
	ds_read_b128 v[78:81], v67 offset:37456
	ds_read_b128 v[82:85], v67 offset:37184
	s_waitcnt lgkmcnt(4)
	v_pk_fma_f32 v[58:59], v[30:31], v[58:59], v[116:117] op_sel_hi:[0,1,1]
	v_pk_fma_f32 v[50:51], v[26:27], v[96:97], v[42:43] op_sel:[1,0,0]
	s_waitcnt lgkmcnt(3)
	v_pk_fma_f32 v[58:59], v[30:31], v[62:63], v[58:59] op_sel:[1,0,0]
	ds_read_b128 v[62:65], v67 offset:37712
	ds_read_b128 v[86:89], v67 offset:37440
	ds_read_b128 v[90:93], v67 offset:37968
	ds_read_b128 v[94:97], v67 offset:38224
	ds_read_b128 v[98:101], v67 offset:37696
	s_waitcnt lgkmcnt(6)
	v_pk_fma_f32 v[58:59], v[32:33], v[80:81], v[58:59] op_sel_hi:[0,1,1]
	v_pk_fma_f32 v[56:57], v[30:31], v[56:57], v[114:115] op_sel_hi:[0,1,1]
	s_waitcnt lgkmcnt(4)
	v_pk_fma_f32 v[58:59], v[40:41], v[64:65], v[58:59] op_sel_hi:[0,1,1]
	s_waitcnt lgkmcnt(2)
	v_pk_fma_f32 v[58:59], v[26:27], v[92:93], v[58:59] op_sel_hi:[0,1,1]
	v_pk_fma_f32 v[56:57], v[30:31], v[60:61], v[56:57] op_sel:[1,0,0]
	s_waitcnt lgkmcnt(1)
	v_pk_fma_f32 v[64:65], v[26:27], v[96:97], v[58:59] op_sel:[1,0,0]
	v_pk_fma_f32 v[60:61], v[32:33], v[78:79], v[56:57] op_sel_hi:[0,1,1]
	ds_read_b128 v[56:59], v67 offset:38480
	v_pk_fma_f32 v[60:61], v[40:41], v[62:63], v[60:61] op_sel_hi:[0,1,1]
	v_pk_fma_f32 v[60:61], v[26:27], v[90:91], v[60:61] op_sel_hi:[0,1,1]
	v_pk_fma_f32 v[78:79], v[26:27], v[94:95], v[60:61] op_sel:[1,0,0]
	ds_read_b128 v[102:105], v67 offset:37952
	s_waitcnt lgkmcnt(1)
	v_pk_fma_f32 v[124:125], v[28:29], v[56:57], v[78:79] op_sel_hi:[0,1,1]
	v_pk_fma_f32 v[56:57], v[30:31], v[76:77], v[112:113] op_sel_hi:[0,1,1]
	v_pk_fma_f32 v[56:57], v[30:31], v[84:85], v[56:57] op_sel:[1,0,0]
	v_pk_fma_f32 v[126:127], v[28:29], v[58:59], v[64:65] op_sel_hi:[0,1,1]
	v_pk_fma_f32 v[56:57], v[32:33], v[88:89], v[56:57] op_sel_hi:[0,1,1]
	v_pk_fma_f32 v[64:65], v[40:41], v[100:101], v[56:57] op_sel_hi:[0,1,1]
	ds_read_b128 v[56:59], v67 offset:38496
	ds_read_b128 v[76:79], v67 offset:38512
	ds_read_b128 v[106:109], v67 offset:38208
	ds_read_b128 v[60:63], v67 offset:38464
	v_mov_b32_e32 v42, v29
	s_waitcnt lgkmcnt(3)
	v_pk_fma_f32 v[118:119], v[28:29], v[56:57], v[118:119] op_sel_hi:[0,1,1]
	s_waitcnt lgkmcnt(2)
	v_pk_fma_f32 v[130:131], v[28:29], v[78:79], v[50:51] op_sel_hi:[0,1,1]
	v_pk_fma_f32 v[50:51], v[30:31], v[74:75], v[110:111] op_sel_hi:[0,1,1]
	v_pk_fma_f32 v[50:51], v[30:31], v[82:83], v[50:51] op_sel:[1,0,0]
	v_pk_fma_f32 v[120:121], v[28:29], v[58:59], v[120:121] op_sel_hi:[0,1,1]
	v_pk_fma_f32 v[50:51], v[32:33], v[86:87], v[50:51] op_sel_hi:[0,1,1]
	v_pk_fma_f32 v[50:51], v[40:41], v[98:99], v[50:51] op_sel_hi:[0,1,1]
	ds_read_b128 v[56:59], v67 offset:36912
	v_pk_fma_f32 v[64:65], v[26:27], v[104:105], v[64:65] op_sel_hi:[0,1,1]
	v_pk_fma_f32 v[50:51], v[26:27], v[102:103], v[50:51] op_sel_hi:[0,1,1]
	s_waitcnt lgkmcnt(2)
	v_pk_fma_f32 v[64:65], v[26:27], v[108:109], v[64:65] op_sel:[1,0,0]
	v_pk_fma_f32 v[50:51], v[26:27], v[106:107], v[50:51] op_sel:[1,0,0]
	s_waitcnt lgkmcnt(1)
	v_pk_fma_f32 v[128:129], v[28:29], v[62:63], v[64:65] op_sel_hi:[0,1,1]
	v_pk_fma_f32 v[122:123], v[28:29], v[76:77], v[122:123] op_sel_hi:[0,1,1]
	v_pk_fma_f32 v[132:133], v[28:29], v[60:61], v[50:51] op_sel_hi:[0,1,1]
	ds_read_b128 v[60:63], v67 offset:37168
	ds_read_b128 v[74:77], v67 offset:36896
	s_waitcnt lgkmcnt(2)
	v_pk_fma_f32 v[50:51], v[30:31], v[58:59], v[54:55] op_sel_hi:[0,1,1]
	ds_read_b128 v[78:81], v67 offset:37424
	ds_read_b128 v[82:85], v67 offset:37152
	s_waitcnt lgkmcnt(3)
	v_pk_fma_f32 v[50:51], v[30:31], v[62:63], v[50:51] op_sel:[1,0,0]
	ds_read_b128 v[62:65], v67 offset:37680
	ds_read_b128 v[86:89], v67 offset:37408
	ds_read_b128 v[90:93], v67 offset:37936
	ds_read_b128 v[94:97], v67 offset:37664
	s_waitcnt lgkmcnt(5)
	v_pk_fma_f32 v[50:51], v[32:33], v[80:81], v[50:51] op_sel_hi:[0,1,1]
	ds_read_b128 v[98:101], v67 offset:38192
	ds_read_b128 v[102:105], v67 offset:38448
	ds_read_b128 v[106:109], v67 offset:37920
	s_waitcnt lgkmcnt(6)
	v_pk_fma_f32 v[50:51], v[40:41], v[64:65], v[50:51] op_sel_hi:[0,1,1]
	s_waitcnt lgkmcnt(4)
	v_pk_fma_f32 v[50:51], v[26:27], v[92:93], v[50:51] op_sel_hi:[0,1,1]
	s_waitcnt lgkmcnt(2)
	v_pk_fma_f32 v[50:51], v[26:27], v[100:101], v[50:51] op_sel:[1,0,0]
	ds_read_b128 v[110:113], v67 offset:38176
	ds_read_b128 v[114:117], v67 offset:38432
	s_waitcnt lgkmcnt(3)
	v_pk_fma_f32 v[64:65], v[28:29], v[104:105], v[50:51] op_sel_hi:[0,1,1]
	v_pk_fma_f32 v[50:51], v[30:31], v[56:57], v[52:53] op_sel_hi:[0,1,1]
	v_pk_fma_f32 v[50:51], v[30:31], v[60:61], v[50:51] op_sel:[1,0,0]
	v_pk_fma_f32 v[48:49], v[30:31], v[76:77], v[48:49] op_sel_hi:[0,1,1]
	v_pk_fma_f32 v[50:51], v[32:33], v[78:79], v[50:51] op_sel_hi:[0,1,1]
	v_pk_fma_f32 v[50:51], v[40:41], v[62:63], v[50:51] op_sel_hi:[0,1,1]
	v_pk_fma_f32 v[54:55], v[26:27], v[90:91], v[50:51] op_sel_hi:[0,1,1]
	ds_read_b128 v[50:53], v67 offset:38704
	v_pk_fma_f32 v[54:55], v[26:27], v[98:99], v[54:55] op_sel:[1,0,0]
	v_pk_fma_f32 v[48:49], v[30:31], v[84:85], v[48:49] op_sel:[1,0,0]
	v_pk_fma_f32 v[62:63], v[28:29], v[102:103], v[54:55] op_sel_hi:[0,1,1]
	ds_read_b128 v[54:57], v67 offset:38720
	ds_read_b128 v[58:61], v67 offset:38688
	v_pk_fma_f32 v[48:49], v[32:33], v[88:89], v[48:49] op_sel_hi:[0,1,1]
	v_pk_fma_f32 v[48:49], v[40:41], v[96:97], v[48:49] op_sel_hi:[0,1,1]
	s_waitcnt lgkmcnt(2)
	v_pk_fma_f32 v[134:135], v[42:43], v[50:51], v[62:63] op_sel_hi:[0,1,1]
	v_pk_fma_f32 v[136:137], v[42:43], v[52:53], v[64:65] op_sel_hi:[0,1,1]
	ds_read_b128 v[50:53], v67 offset:38736
	v_pk_fma_f32 v[48:49], v[26:27], v[108:109], v[48:49] op_sel_hi:[0,1,1]
	v_pk_fma_f32 v[46:47], v[30:31], v[74:75], v[46:47] op_sel_hi:[0,1,1]
	v_pk_fma_f32 v[48:49], v[26:27], v[112:113], v[48:49] op_sel:[1,0,0]
	v_pk_fma_f32 v[46:47], v[30:31], v[82:83], v[46:47] op_sel:[1,0,0]
	s_waitcnt lgkmcnt(2)
	v_pk_fma_f32 v[132:133], v[42:43], v[54:55], v[132:133] op_sel_hi:[0,1,1]
	v_pk_fma_f32 v[138:139], v[42:43], v[56:57], v[128:129] op_sel_hi:[0,1,1]
	v_pk_fma_f32 v[48:49], v[28:29], v[116:117], v[48:49] op_sel_hi:[0,1,1]
	ds_read_b128 v[54:57], v67 offset:38752
	v_pk_fma_f32 v[46:47], v[32:33], v[86:87], v[46:47] op_sel_hi:[0,1,1]
	s_waitcnt lgkmcnt(2)
	v_pk_fma_f32 v[140:141], v[42:43], v[60:61], v[48:49] op_sel_hi:[0,1,1]
	ds_read_b128 v[60:63], v67 offset:38768
	v_pk_fma_f32 v[46:47], v[40:41], v[94:95], v[46:47] op_sel_hi:[0,1,1]
	v_pk_fma_f32 v[46:47], v[26:27], v[106:107], v[46:47] op_sel_hi:[0,1,1]
	s_waitcnt lgkmcnt(2)
	v_pk_fma_f32 v[142:143], v[42:43], v[50:51], v[124:125] op_sel_hi:[0,1,1]
	v_pk_fma_f32 v[50:51], v[26:27], v[110:111], v[46:47] op_sel:[1,0,0]
	ds_read_b128 v[46:49], v67 offset:36880
	v_pk_fma_f32 v[50:51], v[28:29], v[114:115], v[50:51] op_sel_hi:[0,1,1]
	v_pk_fma_f32 v[144:145], v[42:43], v[52:53], v[126:127] op_sel_hi:[0,1,1]
	s_waitcnt lgkmcnt(2)
	v_pk_fma_f32 v[146:147], v[42:43], v[54:55], v[118:119] op_sel_hi:[0,1,1]
	v_pk_fma_f32 v[148:149], v[42:43], v[56:57], v[120:121] op_sel_hi:[0,1,1]
	v_pk_fma_f32 v[152:153], v[42:43], v[58:59], v[50:51] op_sel_hi:[0,1,1]
	ds_read_b128 v[50:53], v67 offset:37136
	ds_read_b128 v[54:57], v67 offset:36864
	s_waitcnt lgkmcnt(3)
	v_pk_fma_f32 v[150:151], v[42:43], v[60:61], v[122:123] op_sel_hi:[0,1,1]
	v_pk_fma_f32 v[130:131], v[42:43], v[62:63], v[130:131] op_sel_hi:[0,1,1]
	ds_read_b128 v[58:61], v67 offset:37392
	ds_read_b128 v[62:65], v67 offset:37120
	ds_read_b128 v[74:77], v67 offset:37648
	ds_read_b128 v[78:81], v67 offset:37376
	s_waitcnt lgkmcnt(6)
	v_pk_fma_f32 v[44:45], v[30:31], v[48:49], v[44:45] op_sel_hi:[0,1,1]
	ds_read_b128 v[82:85], v67 offset:37904
	ds_read_b128 v[86:89], v67 offset:37632
	s_waitcnt lgkmcnt(7)
	v_pk_fma_f32 v[44:45], v[30:31], v[52:53], v[44:45] op_sel:[1,0,0]
	ds_read_b128 v[90:93], v67 offset:38160
	ds_read_b128 v[94:97], v67 offset:37888
	s_waitcnt lgkmcnt(7)
	v_pk_fma_f32 v[44:45], v[32:33], v[60:61], v[44:45] op_sel_hi:[0,1,1]
	ds_read_b128 v[98:101], v67 offset:38416
	ds_read_b128 v[102:105], v67 offset:38144
	s_waitcnt lgkmcnt(7)
	v_pk_fma_f32 v[44:45], v[40:41], v[76:77], v[44:45] op_sel_hi:[0,1,1]
	ds_read_b128 v[106:109], v67 offset:38672
	ds_read_b128 v[110:113], v67 offset:38400
	s_waitcnt lgkmcnt(7)
	v_pk_fma_f32 v[44:45], v[26:27], v[84:85], v[44:45] op_sel_hi:[0,1,1]
	s_waitcnt lgkmcnt(5)
	v_pk_fma_f32 v[44:45], v[26:27], v[92:93], v[44:45] op_sel:[1,0,0]
	ds_read_b128 v[114:117], v67 offset:38944
	ds_read_b128 v[118:121], v67 offset:38928
	ds_read_b128 v[122:125], v67 offset:38656
	ds_read_b128 v[126:129], v67 offset:38960
	v_pk_fma_f32 v[38:39], v[30:31], v[46:47], v[38:39] op_sel_hi:[0,1,1]
	s_waitcnt lgkmcnt(7)
	v_pk_fma_f32 v[44:45], v[28:29], v[100:101], v[44:45] op_sel_hi:[0,1,1]
	v_pk_fma_f32 v[38:39], v[30:31], v[50:51], v[38:39] op_sel:[1,0,0]
	s_waitcnt lgkmcnt(5)
	v_pk_fma_f32 v[44:45], v[42:43], v[108:109], v[44:45] op_sel_hi:[0,1,1]
	v_pk_fma_f32 v[38:39], v[32:33], v[58:59], v[38:39] op_sel_hi:[0,1,1]
	v_pk_fma_f32 v[36:37], v[30:31], v[56:57], v[36:37] op_sel_hi:[0,1,1]
	s_waitcnt lgkmcnt(2)
	v_pk_fma_f32 v[100:101], v[22:23], v[120:121], v[44:45] op_sel_hi:[0,1,1]
	ds_read_b128 v[44:47], v67 offset:38992
	ds_read_b128 v[48:51], v67 offset:39008
	v_pk_fma_f32 v[38:39], v[40:41], v[74:75], v[38:39] op_sel_hi:[0,1,1]
	v_pk_fma_f32 v[36:37], v[30:31], v[64:65], v[36:37] op_sel:[1,0,0]
	v_pk_fma_f32 v[38:39], v[26:27], v[82:83], v[38:39] op_sel_hi:[0,1,1]
	v_pk_fma_f32 v[36:37], v[32:33], v[80:81], v[36:37] op_sel_hi:[0,1,1]
	v_pk_fma_f32 v[34:35], v[30:31], v[54:55], v[34:35] op_sel_hi:[0,1,1]
	v_pk_fma_f32 v[38:39], v[26:27], v[90:91], v[38:39] op_sel:[1,0,0]
	v_pk_fma_f32 v[36:37], v[40:41], v[88:89], v[36:37] op_sel_hi:[0,1,1]
	v_pk_fma_f32 v[30:31], v[30:31], v[62:63], v[34:35] op_sel:[1,0,0]
	v_pk_fma_f32 v[38:39], v[28:29], v[98:99], v[38:39] op_sel_hi:[0,1,1]
	v_pk_fma_f32 v[36:37], v[26:27], v[96:97], v[36:37] op_sel_hi:[0,1,1]
	v_pk_fma_f32 v[30:31], v[32:33], v[78:79], v[30:31] op_sel_hi:[0,1,1]
	v_pk_fma_f32 v[52:53], v[22:23], v[114:115], v[152:153] op_sel_hi:[0,1,1]
	v_pk_fma_f32 v[76:77], v[22:23], v[116:117], v[140:141] op_sel_hi:[0,1,1]
	ds_read_b128 v[114:117], v67 offset:38976
	s_waitcnt lgkmcnt(3)
	v_pk_fma_f32 v[84:85], v[22:23], v[126:127], v[134:135] op_sel_hi:[0,1,1]
	v_pk_fma_f32 v[92:93], v[22:23], v[128:129], v[136:137] op_sel_hi:[0,1,1]
	ds_read_b128 v[126:129], v67 offset:38912
	v_pk_fma_f32 v[38:39], v[42:43], v[106:107], v[38:39] op_sel_hi:[0,1,1]
	v_pk_fma_f32 v[36:37], v[26:27], v[104:105], v[36:37] op_sel:[1,0,0]
	v_pk_fma_f32 v[30:31], v[40:41], v[86:87], v[30:31] op_sel_hi:[0,1,1]
	v_pk_fma_f32 v[74:75], v[22:23], v[118:119], v[38:39] op_sel_hi:[0,1,1]
	ds_read_b128 v[58:61], v67 offset:39024
	s_waitcnt lgkmcnt(4)
	v_pk_fma_f32 v[90:91], v[22:23], v[44:45], v[142:143] op_sel_hi:[0,1,1]
	v_pk_fma_f32 v[98:99], v[22:23], v[46:47], v[144:145] op_sel_hi:[0,1,1]
	s_waitcnt lgkmcnt(3)
	v_pk_fma_f32 v[106:107], v[22:23], v[48:49], v[146:147] op_sel_hi:[0,1,1]
	v_pk_fma_f32 v[48:49], v[28:29], v[112:113], v[36:37] op_sel_hi:[0,1,1]
	ds_read_b128 v[36:39], v67 offset:39168
	ds_read_b128 v[44:47], v67 offset:39184
	v_pk_fma_f32 v[30:31], v[26:27], v[94:95], v[30:31] op_sel_hi:[0,1,1]
	v_pk_fma_f32 v[26:27], v[26:27], v[102:103], v[30:31] op_sel:[1,0,0]
	v_pk_fma_f32 v[48:49], v[42:43], v[124:125], v[48:49] op_sel_hi:[0,1,1]
	v_pk_fma_f32 v[26:27], v[28:29], v[110:111], v[26:27] op_sel_hi:[0,1,1]
	v_pk_fma_f32 v[26:27], v[42:43], v[122:123], v[26:27] op_sel_hi:[0,1,1]
	s_waitcnt lgkmcnt(3)
	v_pk_fma_f32 v[56:57], v[22:23], v[128:129], v[48:49] op_sel_hi:[0,1,1]
	v_pk_fma_f32 v[30:31], v[22:23], v[126:127], v[26:27] op_sel_hi:[0,1,1]
	v_pk_fma_f32 v[108:109], v[22:23], v[114:115], v[132:133] op_sel_hi:[0,1,1]
	v_pk_fma_f32 v[114:115], v[22:23], v[50:51], v[148:149] op_sel_hi:[0,1,1]
	ds_read_b128 v[48:51], v67 offset:39200
	s_waitcnt lgkmcnt(2)
	v_pk_fma_f32 v[38:39], v[22:23], v[38:39], v[56:57] op_sel:[1,0,0]
	s_waitcnt lgkmcnt(1)
	v_pk_fma_f32 v[56:57], v[22:23], v[44:45], v[74:75] op_sel:[1,0,0]
	v_pk_fma_f32 v[64:65], v[22:23], v[46:47], v[100:101] op_sel:[1,0,0]
	ds_read_b128 v[44:47], v67 offset:39216
	ds_read_b128 v[26:29], v67 offset:39232
	v_pk_fma_f32 v[40:41], v[22:23], v[36:37], v[30:31] op_sel:[1,0,0]
	ds_read_b128 v[30:33], v67 offset:39248
	ds_read_b128 v[34:37], v67 offset:39264
	v_pk_fma_f32 v[82:83], v[22:23], v[116:117], v[138:139] op_sel_hi:[0,1,1]
	s_waitcnt lgkmcnt(4)
	v_pk_fma_f32 v[48:49], v[22:23], v[48:49], v[52:53] op_sel:[1,0,0]
	v_pk_fma_f32 v[50:51], v[22:23], v[50:51], v[76:77] op_sel:[1,0,0]
	s_waitcnt lgkmcnt(3)
	v_pk_fma_f32 v[42:43], v[22:23], v[44:45], v[84:85] op_sel:[1,0,0]
	v_pk_fma_f32 v[44:45], v[22:23], v[46:47], v[92:93] op_sel:[1,0,0]
	s_waitcnt lgkmcnt(2)
	v_pk_fma_f32 v[46:47], v[22:23], v[26:27], v[108:109] op_sel:[1,0,0]
	v_pk_fma_f32 v[52:53], v[22:23], v[28:29], v[82:83] op_sel:[1,0,0]
	s_waitcnt lgkmcnt(1)
	v_pk_fma_f32 v[54:55], v[22:23], v[30:31], v[90:91] op_sel:[1,0,0]
	ds_read_b128 v[26:29], v67 offset:39280
	v_pk_fma_f32 v[62:63], v[22:23], v[32:33], v[98:99] op_sel:[1,0,0]
	s_waitcnt lgkmcnt(1)
	v_pk_fma_f32 v[74:75], v[22:23], v[34:35], v[106:107] op_sel:[1,0,0]
	ds_read_b128 v[30:33], v67 offset:39424
	v_pk_fma_f32 v[76:77], v[22:23], v[36:37], v[114:115] op_sel:[1,0,0]
	ds_read_b128 v[34:37], v67 offset:39440
	v_pk_fma_f32 v[58:59], v[22:23], v[58:59], v[150:151] op_sel_hi:[0,1,1]
	v_pk_fma_f32 v[60:61], v[22:23], v[60:61], v[130:131] op_sel_hi:[0,1,1]
	s_waitcnt lgkmcnt(2)
	v_pk_fma_f32 v[58:59], v[22:23], v[26:27], v[58:59] op_sel:[1,0,0]
	v_pk_fma_f32 v[22:23], v[22:23], v[28:29], v[60:61] op_sel:[1,0,0]
	s_waitcnt lgkmcnt(1)
	v_pk_fma_f32 v[60:61], v[24:25], v[30:31], v[40:41] op_sel_hi:[0,1,1]
	ds_read_b128 v[26:29], v67 offset:39456
	v_pk_fma_f32 v[102:103], v[24:25], v[32:33], v[38:39] op_sel_hi:[0,1,1]
	s_waitcnt lgkmcnt(1)
	v_pk_fma_f32 v[104:105], v[24:25], v[34:35], v[56:57] op_sel_hi:[0,1,1]
	ds_read_b128 v[30:33], v67 offset:39472
	v_pk_fma_f32 v[64:65], v[24:25], v[36:37], v[64:65] op_sel_hi:[0,1,1]
	ds_read_b128 v[34:37], v67 offset:39488
	s_waitcnt lgkmcnt(2)
	v_pk_fma_f32 v[106:107], v[24:25], v[26:27], v[48:49] op_sel_hi:[0,1,1]
	v_pk_fma_f32 v[108:109], v[24:25], v[28:29], v[50:51] op_sel_hi:[0,1,1]
	s_waitcnt lgkmcnt(1)
	v_pk_fma_f32 v[110:111], v[24:25], v[30:31], v[42:43] op_sel_hi:[0,1,1]
	v_pk_fma_f32 v[112:113], v[24:25], v[32:33], v[44:45] op_sel_hi:[0,1,1]
	ds_read_b128 v[26:29], v67 offset:39504
	s_waitcnt lgkmcnt(1)
	v_pk_fma_f32 v[42:43], v[24:25], v[34:35], v[46:47] op_sel_hi:[0,1,1]
	ds_read_b128 v[30:33], v67 offset:39520
	ds_read_b128 v[44:47], v67 offset:39536
	ds_read_b128 v[48:51], v67 offset:39680
	v_pk_fma_f32 v[40:41], v[24:25], v[36:37], v[52:53] op_sel_hi:[0,1,1]
	s_waitcnt lgkmcnt(3)
	v_pk_fma_f32 v[38:39], v[24:25], v[26:27], v[54:55] op_sel_hi:[0,1,1]
	v_pk_fma_f32 v[36:37], v[24:25], v[28:29], v[62:63] op_sel_hi:[0,1,1]
	s_waitcnt lgkmcnt(1)
	v_pk_fma_f32 v[26:27], v[24:25], v[44:45], v[58:59] op_sel_hi:[0,1,1]
	v_pk_fma_f32 v[22:23], v[24:25], v[46:47], v[22:23] op_sel_hi:[0,1,1]
	ds_read_b128 v[44:47], v67 offset:39936
	ds_read_b128 v[52:55], v67 offset:39696
	v_pk_fma_f32 v[34:35], v[24:25], v[30:31], v[74:75] op_sel_hi:[0,1,1]
	v_pk_fma_f32 v[28:29], v[24:25], v[32:33], v[76:77] op_sel_hi:[0,1,1]
	v_mov_b32_e32 v24, v25
	s_waitcnt lgkmcnt(2)
	v_pk_fma_f32 v[30:31], v[24:25], v[48:49], v[60:61] op_sel_hi:[0,1,1]
	ds_read_b128 v[56:59], v67 offset:40192
	ds_read_b128 v[60:63], v67 offset:39952
	ds_read_b128 v[74:77], v67 offset:40448
	ds_read_b128 v[78:81], v67 offset:40208
	s_waitcnt lgkmcnt(5)
	v_pk_fma_f32 v[30:31], v[18:19], v[44:45], v[30:31] op_sel_hi:[0,1,1]
	ds_read_b128 v[82:85], v67 offset:40704
	ds_read_b128 v[86:89], v67 offset:40464
	ds_read_b128 v[90:93], v67 offset:40960
	ds_read_b128 v[94:97], v67 offset:40720
	v_pk_fma_f32 v[44:45], v[24:25], v[50:51], v[102:103] op_sel_hi:[0,1,1]
	v_pk_fma_f32 v[44:45], v[18:19], v[46:47], v[44:45] op_sel_hi:[0,1,1]
	s_waitcnt lgkmcnt(7)
	v_pk_fma_f32 v[30:31], v[18:19], v[56:57], v[30:31] op_sel:[1,0,0]
	v_pk_fma_f32 v[44:45], v[18:19], v[58:59], v[44:45] op_sel:[1,0,0]
	s_waitcnt lgkmcnt(5)
	v_pk_fma_f32 v[32:33], v[20:21], v[74:75], v[30:31] op_sel_hi:[0,1,1]
	v_mov_b32_e32 v30, v21
	v_pk_fma_f32 v[44:45], v[20:21], v[76:77], v[44:45] op_sel_hi:[0,1,1]
	s_waitcnt lgkmcnt(3)
	v_pk_fma_f32 v[44:45], v[30:31], v[84:85], v[44:45] op_sel_hi:[0,1,1]
	ds_read_b128 v[98:101], v67 offset:40976
	s_waitcnt lgkmcnt(2)
	v_pk_fma_f32 v[102:103], v[14:15], v[92:93], v[44:45] op_sel_hi:[0,1,1]
	v_pk_fma_f32 v[44:45], v[24:25], v[52:53], v[104:105] op_sel_hi:[0,1,1]
	v_pk_fma_f32 v[44:45], v[18:19], v[60:61], v[44:45] op_sel_hi:[0,1,1]
	v_pk_fma_f32 v[44:45], v[18:19], v[78:79], v[44:45] op_sel:[1,0,0]
	v_pk_fma_f32 v[32:33], v[30:31], v[82:83], v[32:33] op_sel_hi:[0,1,1]
	v_pk_fma_f32 v[44:45], v[20:21], v[86:87], v[44:45] op_sel_hi:[0,1,1]
	s_waitcnt lgkmcnt(1)
	v_pk_fma_f32 v[44:45], v[30:31], v[94:95], v[44:45] op_sel_hi:[0,1,1]
	s_waitcnt lgkmcnt(0)
	v_pk_fma_f32 v[104:105], v[14:15], v[98:99], v[44:45] op_sel_hi:[0,1,1]
	v_pk_fma_f32 v[44:45], v[24:25], v[54:55], v[64:65] op_sel_hi:[0,1,1]
	v_pk_fma_f32 v[44:45], v[18:19], v[62:63], v[44:45] op_sel_hi:[0,1,1]
	v_pk_fma_f32 v[44:45], v[18:19], v[80:81], v[44:45] op_sel:[1,0,0]
	v_pk_fma_f32 v[114:115], v[14:15], v[90:91], v[32:33] op_sel_hi:[0,1,1]
	v_pk_fma_f32 v[48:49], v[20:21], v[88:89], v[44:45] op_sel_hi:[0,1,1]
	ds_read_b128 v[44:47], v67 offset:39712
	v_pk_fma_f32 v[48:49], v[30:31], v[96:97], v[48:49] op_sel_hi:[0,1,1]
	v_pk_fma_f32 v[64:65], v[14:15], v[100:101], v[48:49] op_sel_hi:[0,1,1]
	ds_read_b128 v[48:51], v67 offset:39968
	ds_read_b128 v[52:55], v67 offset:39728
	ds_read_b128 v[56:59], v67 offset:40224
	ds_read_b128 v[60:63], v67 offset:39984
	ds_read_b128 v[74:77], v67 offset:40480
	ds_read_b128 v[78:81], v67 offset:40240
	s_waitcnt lgkmcnt(6)
	v_pk_fma_f32 v[44:45], v[24:25], v[44:45], v[106:107] op_sel_hi:[0,1,1]
	s_waitcnt lgkmcnt(5)
	v_pk_fma_f32 v[44:45], v[18:19], v[48:49], v[44:45] op_sel_hi:[0,1,1]
	ds_read_b128 v[82:85], v67 offset:40736
	ds_read_b128 v[86:89], v67 offset:40992
	ds_read_b128 v[90:93], v67 offset:40496
	s_waitcnt lgkmcnt(6)
	v_pk_fma_f32 v[44:45], v[18:19], v[56:57], v[44:45] op_sel:[1,0,0]
	ds_read_b128 v[94:97], v67 offset:40752
	ds_read_b128 v[98:101], v67 offset:41008
	s_waitcnt lgkmcnt(6)
	v_pk_fma_f32 v[44:45], v[20:21], v[74:75], v[44:45] op_sel_hi:[0,1,1]
	s_waitcnt lgkmcnt(4)
	v_pk_fma_f32 v[44:45], v[30:31], v[82:83], v[44:45] op_sel_hi:[0,1,1]
	s_waitcnt lgkmcnt(3)
	v_pk_fma_f32 v[56:57], v[14:15], v[86:87], v[44:45] op_sel_hi:[0,1,1]
	v_pk_fma_f32 v[44:45], v[24:25], v[46:47], v[108:109] op_sel_hi:[0,1,1]
	v_pk_fma_f32 v[44:45], v[18:19], v[50:51], v[44:45] op_sel_hi:[0,1,1]
	v_pk_fma_f32 v[48:49], v[18:19], v[58:59], v[44:45] op_sel:[1,0,0]
	ds_read_b128 v[44:47], v67 offset:41216
	v_pk_fma_f32 v[58:59], v[20:21], v[76:77], v[48:49] op_sel_hi:[0,1,1]
	ds_read_b128 v[48:51], v67 offset:41232
	v_pk_fma_f32 v[58:59], v[30:31], v[84:85], v[58:59] op_sel_hi:[0,1,1]
	v_pk_fma_f32 v[58:59], v[14:15], v[88:89], v[58:59] op_sel_hi:[0,1,1]
	s_waitcnt lgkmcnt(1)
	v_pk_fma_f32 v[106:107], v[14:15], v[44:45], v[114:115] op_sel:[1,0,0]
	v_pk_fma_f32 v[44:45], v[24:25], v[52:53], v[110:111] op_sel_hi:[0,1,1]
	v_pk_fma_f32 v[44:45], v[18:19], v[60:61], v[44:45] op_sel_hi:[0,1,1]
	v_pk_fma_f32 v[108:109], v[14:15], v[46:47], v[102:103] op_sel:[1,0,0]
	s_waitcnt lgkmcnt(0)
	v_pk_fma_f32 v[114:115], v[14:15], v[48:49], v[104:105] op_sel:[1,0,0]
	v_pk_fma_f32 v[48:49], v[18:19], v[78:79], v[44:45] op_sel:[1,0,0]
	ds_read_b128 v[44:47], v67 offset:41248
	v_pk_fma_f32 v[64:65], v[14:15], v[50:51], v[64:65] op_sel:[1,0,0]
	v_pk_fma_f32 v[52:53], v[20:21], v[90:91], v[48:49] op_sel_hi:[0,1,1]
	ds_read_b128 v[48:51], v67 offset:41264
	v_pk_fma_f32 v[52:53], v[30:31], v[94:95], v[52:53] op_sel_hi:[0,1,1]
	s_waitcnt lgkmcnt(1)
	v_pk_fma_f32 v[110:111], v[14:15], v[44:45], v[56:57] op_sel:[1,0,0]
	v_pk_fma_f32 v[44:45], v[24:25], v[54:55], v[112:113] op_sel_hi:[0,1,1]
	v_pk_fma_f32 v[44:45], v[18:19], v[62:63], v[44:45] op_sel_hi:[0,1,1]
	v_pk_fma_f32 v[44:45], v[18:19], v[80:81], v[44:45] op_sel:[1,0,0]
	v_pk_fma_f32 v[52:53], v[14:15], v[98:99], v[52:53] op_sel_hi:[0,1,1]
	v_pk_fma_f32 v[44:45], v[20:21], v[92:93], v[44:45] op_sel_hi:[0,1,1]
	v_pk_fma_f32 v[116:117], v[14:15], v[46:47], v[58:59] op_sel:[1,0,0]
	s_waitcnt lgkmcnt(0)
	v_pk_fma_f32 v[118:119], v[14:15], v[48:49], v[52:53] op_sel:[1,0,0]
	v_pk_fma_f32 v[48:49], v[30:31], v[96:97], v[44:45] op_sel_hi:[0,1,1]
	ds_read_b128 v[44:47], v67 offset:39744
	v_pk_fma_f32 v[48:49], v[14:15], v[100:101], v[48:49] op_sel_hi:[0,1,1]
	v_pk_fma_f32 v[112:113], v[14:15], v[50:51], v[48:49] op_sel:[1,0,0]
	ds_read_b128 v[48:51], v67 offset:40000
	ds_read_b128 v[52:55], v67 offset:39760
	v_mov_b32_e32 v32, v17
	s_waitcnt lgkmcnt(2)
	v_pk_fma_f32 v[60:61], v[24:25], v[44:45], v[42:43] op_sel_hi:[0,1,1]
	ds_read_b128 v[42:45], v67 offset:40256
	ds_read_b128 v[56:59], v67 offset:40016
	s_waitcnt lgkmcnt(3)
	v_pk_fma_f32 v[48:49], v[18:19], v[48:49], v[60:61] op_sel_hi:[0,1,1]
	ds_read_b128 v[60:63], v67 offset:40512
	ds_read_b128 v[74:77], v67 offset:40272
	ds_read_b128 v[78:81], v67 offset:40768
	ds_read_b128 v[82:85], v67 offset:40528
	v_pk_fma_f32 v[40:41], v[24:25], v[46:47], v[40:41] op_sel_hi:[0,1,1]
	v_pk_fma_f32 v[40:41], v[18:19], v[50:51], v[40:41] op_sel_hi:[0,1,1]
	s_waitcnt lgkmcnt(5)
	v_pk_fma_f32 v[42:43], v[18:19], v[42:43], v[48:49] op_sel:[1,0,0]
	ds_read_b128 v[86:89], v67 offset:41024
	ds_read_b128 v[90:93], v67 offset:41280
	ds_read_b128 v[94:97], v67 offset:40784
	v_pk_fma_f32 v[40:41], v[18:19], v[44:45], v[40:41] op_sel:[1,0,0]
	s_waitcnt lgkmcnt(6)
	v_pk_fma_f32 v[42:43], v[20:21], v[60:61], v[42:43] op_sel_hi:[0,1,1]
	v_pk_fma_f32 v[44:45], v[20:21], v[62:63], v[40:41] op_sel_hi:[0,1,1]
	s_waitcnt lgkmcnt(4)
	v_pk_fma_f32 v[42:43], v[30:31], v[78:79], v[42:43] op_sel_hi:[0,1,1]
	v_pk_fma_f32 v[44:45], v[30:31], v[80:81], v[44:45] op_sel_hi:[0,1,1]
	s_waitcnt lgkmcnt(2)
	v_pk_fma_f32 v[42:43], v[14:15], v[86:87], v[42:43] op_sel_hi:[0,1,1]
	v_pk_fma_f32 v[48:49], v[14:15], v[88:89], v[44:45] op_sel_hi:[0,1,1]
	s_waitcnt lgkmcnt(1)
	v_pk_fma_f32 v[60:61], v[14:15], v[90:91], v[42:43] op_sel:[1,0,0]
	ds_read_b128 v[40:43], v67 offset:41472
	v_pk_fma_f32 v[62:63], v[14:15], v[92:93], v[48:49] op_sel:[1,0,0]
	ds_read_b128 v[48:51], v67 offset:41504
	ds_read_b128 v[98:101], v67 offset:41040
	ds_read_b128 v[102:105], v67 offset:41296
	v_pk_fma_f32 v[38:39], v[24:25], v[52:53], v[38:39] op_sel_hi:[0,1,1]
	v_pk_fma_f32 v[38:39], v[18:19], v[56:57], v[38:39] op_sel_hi:[0,1,1]
	ds_read_b128 v[44:47], v67 offset:41488
	s_waitcnt lgkmcnt(4)
	v_pk_fma_f32 v[120:121], v[16:17], v[40:41], v[106:107] op_sel_hi:[0,1,1]
	v_pk_fma_f32 v[122:123], v[16:17], v[42:43], v[108:109] op_sel_hi:[0,1,1]
	ds_read_b128 v[40:43], v67 offset:41520
	s_waitcnt lgkmcnt(4)
	v_pk_fma_f32 v[126:127], v[16:17], v[48:49], v[110:111] op_sel_hi:[0,1,1]
	v_pk_fma_f32 v[128:129], v[16:17], v[50:51], v[116:117] op_sel_hi:[0,1,1]
	v_pk_fma_f32 v[38:39], v[18:19], v[74:75], v[38:39] op_sel:[1,0,0]
	ds_read_b128 v[48:51], v67 offset:41552
	v_pk_fma_f32 v[36:37], v[24:25], v[54:55], v[36:37] op_sel_hi:[0,1,1]
	v_pk_fma_f32 v[38:39], v[20:21], v[82:83], v[38:39] op_sel_hi:[0,1,1]
	v_pk_fma_f32 v[36:37], v[18:19], v[58:59], v[36:37] op_sel_hi:[0,1,1]
	v_pk_fma_f32 v[38:39], v[30:31], v[94:95], v[38:39] op_sel_hi:[0,1,1]
	v_pk_fma_f32 v[36:37], v[18:19], v[76:77], v[36:37] op_sel:[1,0,0]
	s_waitcnt lgkmcnt(4)
	v_pk_fma_f32 v[38:39], v[14:15], v[98:99], v[38:39] op_sel_hi:[0,1,1]
	v_pk_fma_f32 v[36:37], v[20:21], v[84:85], v[36:37] op_sel_hi:[0,1,1]
	s_waitcnt lgkmcnt(3)
	v_pk_fma_f32 v[38:39], v[14:15], v[102:103], v[38:39] op_sel:[1,0,0]
	v_pk_fma_f32 v[36:37], v[30:31], v[96:97], v[36:37] op_sel_hi:[0,1,1]
	s_waitcnt lgkmcnt(1)
	v_pk_fma_f32 v[118:119], v[16:17], v[40:41], v[118:119] op_sel_hi:[0,1,1]
	s_waitcnt lgkmcnt(0)
	v_pk_fma_f32 v[136:137], v[16:17], v[48:49], v[38:39] op_sel_hi:[0,1,1]
	v_pk_fma_f32 v[40:41], v[14:15], v[100:101], v[36:37] op_sel_hi:[0,1,1]
	ds_read_b128 v[36:39], v67 offset:39776
	v_pk_fma_f32 v[124:125], v[16:17], v[44:45], v[114:115] op_sel_hi:[0,1,1]
	v_pk_fma_f32 v[64:65], v[16:17], v[46:47], v[64:65] op_sel_hi:[0,1,1]
	ds_read_b128 v[44:47], v67 offset:41536
	v_pk_fma_f32 v[40:41], v[14:15], v[104:105], v[40:41] op_sel:[1,0,0]
	v_pk_fma_f32 v[130:131], v[16:17], v[42:43], v[112:113] op_sel_hi:[0,1,1]
	v_pk_fma_f32 v[138:139], v[16:17], v[50:51], v[40:41] op_sel_hi:[0,1,1]
	s_waitcnt lgkmcnt(1)
	v_pk_fma_f32 v[52:53], v[24:25], v[36:37], v[34:35] op_sel_hi:[0,1,1]
	s_waitcnt lgkmcnt(0)
	v_pk_fma_f32 v[132:133], v[16:17], v[44:45], v[60:61] op_sel_hi:[0,1,1]
	v_pk_fma_f32 v[134:135], v[16:17], v[46:47], v[62:63] op_sel_hi:[0,1,1]
	ds_read_b128 v[40:43], v67 offset:40032
	ds_read_b128 v[44:47], v67 offset:39792
	ds_read_b128 v[34:37], v67 offset:40288
	ds_read_b128 v[48:51], v67 offset:40048
	v_pk_fma_f32 v[28:29], v[24:25], v[38:39], v[28:29] op_sel_hi:[0,1,1]
	s_waitcnt lgkmcnt(3)
	v_pk_fma_f32 v[40:41], v[18:19], v[40:41], v[52:53] op_sel_hi:[0,1,1]
	ds_read_b128 v[52:55], v67 offset:40544
	ds_read_b128 v[56:59], v67 offset:40304
	ds_read_b128 v[60:63], v67 offset:40800
	ds_read_b128 v[74:77], v67 offset:40560
	ds_read_b128 v[78:81], v67 offset:41056
	ds_read_b128 v[82:85], v67 offset:40816
	s_waitcnt lgkmcnt(7)
	v_pk_fma_f32 v[34:35], v[18:19], v[34:35], v[40:41] op_sel:[1,0,0]
	ds_read_b128 v[86:89], v67 offset:41312
	ds_read_b128 v[90:93], v67 offset:41072
	s_waitcnt lgkmcnt(7)
	v_pk_fma_f32 v[34:35], v[20:21], v[52:53], v[34:35] op_sel_hi:[0,1,1]
	s_waitcnt lgkmcnt(5)
	v_pk_fma_f32 v[34:35], v[30:31], v[60:61], v[34:35] op_sel_hi:[0,1,1]
	ds_read_b128 v[94:97], v67 offset:41568
	ds_read_b128 v[98:101], v67 offset:41728
	ds_read_b128 v[102:105], v67 offset:41328
	s_waitcnt lgkmcnt(6)
	v_pk_fma_f32 v[34:35], v[14:15], v[78:79], v[34:35] op_sel_hi:[0,1,1]
	v_pk_fma_f32 v[28:29], v[18:19], v[42:43], v[28:29] op_sel_hi:[0,1,1]
	s_waitcnt lgkmcnt(4)
	v_pk_fma_f32 v[34:35], v[14:15], v[86:87], v[34:35] op_sel:[1,0,0]
	v_pk_fma_f32 v[28:29], v[18:19], v[36:37], v[28:29] op_sel:[1,0,0]
	s_waitcnt lgkmcnt(2)
	v_pk_fma_f32 v[60:61], v[16:17], v[94:95], v[34:35] op_sel_hi:[0,1,1]
	v_pk_fma_f32 v[28:29], v[20:21], v[54:55], v[28:29] op_sel_hi:[0,1,1]
	ds_read_b128 v[34:37], v67 offset:41792
	ds_read_b128 v[38:41], v67 offset:41808
	ds_read_b128 v[52:55], v67 offset:41824
	v_pk_fma_f32 v[26:27], v[24:25], v[44:45], v[26:27] op_sel_hi:[0,1,1]
	v_pk_fma_f32 v[28:29], v[30:31], v[62:63], v[28:29] op_sel_hi:[0,1,1]
	v_pk_fma_f32 v[26:27], v[18:19], v[48:49], v[26:27] op_sel_hi:[0,1,1]
	v_pk_fma_f32 v[28:29], v[14:15], v[80:81], v[28:29] op_sel_hi:[0,1,1]
	v_pk_fma_f32 v[26:27], v[18:19], v[56:57], v[26:27] op_sel:[1,0,0]
	v_pk_fma_f32 v[28:29], v[14:15], v[88:89], v[28:29] op_sel:[1,0,0]
	v_pk_fma_f32 v[26:27], v[20:21], v[74:75], v[26:27] op_sel_hi:[0,1,1]
	ds_read_b128 v[106:109], v67 offset:41584
	ds_read_b128 v[110:113], v67 offset:41744
	v_pk_fma_f32 v[28:29], v[16:17], v[96:97], v[28:29] op_sel_hi:[0,1,1]
	v_pk_fma_f32 v[26:27], v[30:31], v[82:83], v[26:27] op_sel_hi:[0,1,1]
	s_waitcnt lgkmcnt(4)
	v_pk_fma_f32 v[62:63], v[32:33], v[34:35], v[132:133] op_sel_hi:[0,1,1]
	v_pk_fma_f32 v[80:81], v[32:33], v[36:37], v[134:135] op_sel_hi:[0,1,1]
	s_waitcnt lgkmcnt(3)
	v_pk_fma_f32 v[88:89], v[32:33], v[38:39], v[136:137] op_sel_hi:[0,1,1]
	ds_read_b128 v[34:37], v67 offset:41840
	s_waitcnt lgkmcnt(3)
	v_pk_fma_f32 v[54:55], v[32:33], v[54:55], v[28:29] op_sel_hi:[0,1,1]
	v_pk_fma_f32 v[38:39], v[14:15], v[90:91], v[26:27] op_sel_hi:[0,1,1]
	ds_read_b128 v[26:29], v67 offset:41984
	v_pk_fma_f32 v[22:23], v[24:25], v[46:47], v[22:23] op_sel_hi:[0,1,1]
	v_pk_fma_f32 v[38:39], v[14:15], v[102:103], v[38:39] op_sel:[1,0,0]
	v_pk_fma_f32 v[22:23], v[18:19], v[50:51], v[22:23] op_sel_hi:[0,1,1]
	v_pk_fma_f32 v[78:79], v[32:33], v[98:99], v[120:121] op_sel_hi:[0,1,1]
	ds_read_b128 v[114:117], v67 offset:41760
	v_pk_fma_f32 v[86:87], v[32:33], v[100:101], v[122:123] op_sel_hi:[0,1,1]
	ds_read_b128 v[98:101], v67 offset:41776
	s_waitcnt lgkmcnt(5)
	v_pk_fma_f32 v[38:39], v[16:17], v[106:107], v[38:39] op_sel_hi:[0,1,1]
	v_pk_fma_f32 v[18:19], v[18:19], v[58:59], v[22:23] op_sel:[1,0,0]
	v_pk_fma_f32 v[96:97], v[32:33], v[40:41], v[138:139] op_sel_hi:[0,1,1]
	s_waitcnt lgkmcnt(3)
	v_pk_fma_f32 v[34:35], v[32:33], v[34:35], v[38:39] op_sel_hi:[0,1,1]
	ds_read_b128 v[38:41], v67 offset:42000
	s_waitcnt lgkmcnt(3)
	v_pk_fma_f32 v[48:49], v[10:11], v[26:27], v[78:79] op_sel_hi:[0,1,1]
	ds_read_b128 v[42:45], v67 offset:42016
	v_pk_fma_f32 v[56:57], v[10:11], v[28:29], v[86:87] op_sel_hi:[0,1,1]
	ds_read_b128 v[26:29], v67 offset:42032
	v_pk_fma_f32 v[18:19], v[20:21], v[76:77], v[18:19] op_sel_hi:[0,1,1]
	v_pk_fma_f32 v[18:19], v[30:31], v[84:85], v[18:19] op_sel_hi:[0,1,1]
	v_pk_fma_f32 v[18:19], v[14:15], v[92:93], v[18:19] op_sel_hi:[0,1,1]
	v_pk_fma_f32 v[14:15], v[14:15], v[104:105], v[18:19] op_sel:[1,0,0]
	v_pk_fma_f32 v[64:65], v[32:33], v[112:113], v[64:65] op_sel_hi:[0,1,1]
	s_waitcnt lgkmcnt(3)
	v_pk_fma_f32 v[98:99], v[32:33], v[98:99], v[118:119] op_sel_hi:[0,1,1]
	v_pk_fma_f32 v[14:15], v[16:17], v[108:109], v[14:15] op_sel_hi:[0,1,1]
	s_waitcnt lgkmcnt(2)
	v_pk_fma_f32 v[40:41], v[10:11], v[40:41], v[64:65] op_sel_hi:[0,1,1]
	s_waitcnt lgkmcnt(0)
	v_pk_fma_f32 v[64:65], v[10:11], v[26:27], v[98:99] op_sel_hi:[0,1,1]
	ds_read_b128 v[18:21], v67 offset:42048
	v_pk_fma_f32 v[26:27], v[32:33], v[36:37], v[14:15] op_sel_hi:[0,1,1]
	ds_read_b128 v[14:17], v67 offset:42064
	ds_read_b128 v[22:25], v67 offset:42080
	v_pk_fma_f32 v[52:53], v[32:33], v[52:53], v[60:61] op_sel_hi:[0,1,1]
	s_waitcnt lgkmcnt(2)
	v_pk_fma_f32 v[46:47], v[10:11], v[18:19], v[62:63] op_sel_hi:[0,1,1]
	v_pk_fma_f32 v[50:51], v[10:11], v[20:21], v[80:81] op_sel_hi:[0,1,1]
	s_waitcnt lgkmcnt(1)
	v_pk_fma_f32 v[58:59], v[10:11], v[14:15], v[88:89] op_sel_hi:[0,1,1]
	ds_read_b128 v[18:21], v67 offset:42096
	v_pk_fma_f32 v[62:63], v[10:11], v[16:17], v[96:97] op_sel_hi:[0,1,1]
	s_waitcnt lgkmcnt(1)
	v_pk_fma_f32 v[52:53], v[10:11], v[22:23], v[52:53] op_sel_hi:[0,1,1]
	ds_read_b128 v[14:17], v67 offset:42240
	v_pk_fma_f32 v[54:55], v[10:11], v[24:25], v[54:55] op_sel_hi:[0,1,1]
	ds_read_b128 v[22:25], v67 offset:42256
	v_pk_fma_f32 v[94:95], v[32:33], v[110:111], v[124:125] op_sel_hi:[0,1,1]
	v_pk_fma_f32 v[110:111], v[32:33], v[114:115], v[126:127] op_sel_hi:[0,1,1]
	v_pk_fma_f32 v[38:39], v[10:11], v[38:39], v[94:95] op_sel_hi:[0,1,1]
	v_pk_fma_f32 v[60:61], v[10:11], v[42:43], v[110:111] op_sel_hi:[0,1,1]
	s_waitcnt lgkmcnt(2)
	v_pk_fma_f32 v[74:75], v[10:11], v[18:19], v[34:35] op_sel_hi:[0,1,1]
	v_pk_fma_f32 v[76:77], v[10:11], v[20:21], v[26:27] op_sel_hi:[0,1,1]
	s_waitcnt lgkmcnt(1)
	v_pk_fma_f32 v[34:35], v[10:11], v[14:15], v[48:49] op_sel:[1,0,0]
	ds_read_b128 v[18:21], v67 offset:42272
	s_waitcnt lgkmcnt(1)
	v_pk_fma_f32 v[42:43], v[10:11], v[22:23], v[38:39] op_sel:[1,0,0]
	v_pk_fma_f32 v[48:49], v[10:11], v[24:25], v[40:41] op_sel:[1,0,0]
	ds_read_b128 v[22:25], v67 offset:42304
	ds_read_b128 v[38:41], v67 offset:42320
	v_pk_fma_f32 v[100:101], v[32:33], v[100:101], v[130:131] op_sel_hi:[0,1,1]
	v_pk_fma_f32 v[112:113], v[32:33], v[116:117], v[128:129] op_sel_hi:[0,1,1]
	v_pk_fma_f32 v[32:33], v[10:11], v[28:29], v[100:101] op_sel_hi:[0,1,1]
	ds_read_b128 v[26:29], v67 offset:42288
	v_pk_fma_f32 v[44:45], v[10:11], v[44:45], v[112:113] op_sel_hi:[0,1,1]
	s_waitcnt lgkmcnt(3)
	v_pk_fma_f32 v[14:15], v[10:11], v[20:21], v[44:45] op_sel:[1,0,0]
	s_waitcnt lgkmcnt(2)
	v_pk_fma_f32 v[90:91], v[10:11], v[22:23], v[46:47] op_sel:[1,0,0]
	ds_read_b128 v[20:23], v67 offset:42336
	v_pk_fma_f32 v[36:37], v[10:11], v[16:17], v[56:57] op_sel:[1,0,0]
	s_waitcnt lgkmcnt(1)
	v_pk_fma_f32 v[16:17], v[10:11], v[26:27], v[64:65] op_sel:[1,0,0]
	v_pk_fma_f32 v[92:93], v[10:11], v[24:25], v[50:51] op_sel:[1,0,0]
	ds_read_b128 v[24:27], v67 offset:42352
	s_waitcnt lgkmcnt(1)
	v_pk_fma_f32 v[88:89], v[10:11], v[20:21], v[52:53] op_sel:[1,0,0]
	v_pk_fma_f32 v[96:97], v[10:11], v[22:23], v[54:55] op_sel:[1,0,0]
	ds_read_b128 v[20:23], v67 offset:42608
	v_pk_fma_f32 v[30:31], v[10:11], v[18:19], v[60:61] op_sel:[1,0,0]
	v_pk_fma_f32 v[18:19], v[10:11], v[28:29], v[32:33] op_sel:[1,0,0]
	v_pk_fma_f32 v[94:95], v[10:11], v[38:39], v[58:59] op_sel:[1,0,0]
	v_pk_fma_f32 v[86:87], v[10:11], v[40:41], v[62:63] op_sel:[1,0,0]
	s_waitcnt lgkmcnt(1)
	v_pk_fma_f32 v[98:99], v[10:11], v[24:25], v[74:75] op_sel:[1,0,0]
	v_pk_fma_f32 v[10:11], v[10:11], v[26:27], v[76:77] op_sel:[1,0,0]
	ds_read_b128 v[24:27], v67 offset:42864
	ds_read_b128 v[38:41], v67 offset:42592
	s_waitcnt lgkmcnt(2)
	v_pk_fma_f32 v[22:23], v[12:13], v[22:23], v[10:11] op_sel_hi:[0,1,1]
	v_mov_b32_e32 v10, v13
	ds_read_b128 v[44:47], v67 offset:43120
	ds_read_b128 v[52:55], v67 offset:42848
	s_waitcnt lgkmcnt(3)
	v_pk_fma_f32 v[22:23], v[10:11], v[26:27], v[22:23] op_sel_hi:[0,1,1]
	ds_read_b128 v[26:29], v67 offset:43376
	ds_read_b128 v[56:59], v67 offset:43104
	ds_read_b128 v[60:63], v67 offset:43632
	ds_read_b128 v[74:77], v67 offset:43360
	v_pk_fma_f32 v[20:21], v[12:13], v[20:21], v[98:99] op_sel_hi:[0,1,1]
	ds_read_b128 v[78:81], v67 offset:43888
	ds_read_b128 v[82:85], v67 offset:43616
	v_pk_fma_f32 v[20:21], v[10:11], v[24:25], v[20:21] op_sel_hi:[0,1,1]
	s_waitcnt lgkmcnt(7)
	v_pk_fma_f32 v[20:21], v[6:7], v[44:45], v[20:21] op_sel_hi:[0,1,1]
	v_pk_fma_f32 v[22:23], v[6:7], v[46:47], v[22:23] op_sel_hi:[0,1,1]
	s_waitcnt lgkmcnt(5)
	v_pk_fma_f32 v[20:21], v[6:7], v[26:27], v[20:21] op_sel:[1,0,0]
	v_pk_fma_f32 v[22:23], v[6:7], v[28:29], v[22:23] op_sel:[1,0,0]
	v_mov_b32_e32 v50, v9
	s_waitcnt lgkmcnt(3)
	v_pk_fma_f32 v[20:21], v[8:9], v[60:61], v[20:21] op_sel_hi:[0,1,1]
	v_pk_fma_f32 v[22:23], v[8:9], v[62:63], v[22:23] op_sel_hi:[0,1,1]
	ds_read_b128 v[62:65], v67 offset:43872
	s_waitcnt lgkmcnt(2)
	v_pk_fma_f32 v[98:99], v[50:51], v[78:79], v[20:21] op_sel_hi:[0,1,1]
	v_pk_fma_f32 v[20:21], v[12:13], v[40:41], v[96:97] op_sel_hi:[0,1,1]
	v_pk_fma_f32 v[20:21], v[10:11], v[54:55], v[20:21] op_sel_hi:[0,1,1]
	v_pk_fma_f32 v[20:21], v[6:7], v[58:59], v[20:21] op_sel_hi:[0,1,1]
	v_pk_fma_f32 v[20:21], v[6:7], v[76:77], v[20:21] op_sel:[1,0,0]
	v_pk_fma_f32 v[100:101], v[50:51], v[80:81], v[22:23] op_sel_hi:[0,1,1]
	s_waitcnt lgkmcnt(1)
	v_pk_fma_f32 v[20:21], v[8:9], v[84:85], v[20:21] op_sel_hi:[0,1,1]
	s_waitcnt lgkmcnt(0)
	v_pk_fma_f32 v[64:65], v[50:51], v[64:65], v[20:21] op_sel_hi:[0,1,1]
	v_pk_fma_f32 v[20:21], v[12:13], v[38:39], v[88:89] op_sel_hi:[0,1,1]
	v_pk_fma_f32 v[20:21], v[10:11], v[52:53], v[20:21] op_sel_hi:[0,1,1]
	v_pk_fma_f32 v[20:21], v[6:7], v[56:57], v[20:21] op_sel_hi:[0,1,1]
	v_pk_fma_f32 v[24:25], v[6:7], v[74:75], v[20:21] op_sel:[1,0,0]
	ds_read_b128 v[20:23], v67 offset:42576
	v_pk_fma_f32 v[24:25], v[8:9], v[82:83], v[24:25] op_sel_hi:[0,1,1]
	v_pk_fma_f32 v[96:97], v[50:51], v[62:63], v[24:25] op_sel_hi:[0,1,1]
	ds_read_b128 v[24:27], v67 offset:42832
	ds_read_b128 v[52:55], v67 offset:42560
	ds_read_b128 v[38:41], v67 offset:43088
	ds_read_b128 v[56:59], v67 offset:42816
	s_waitcnt lgkmcnt(4)
	v_pk_fma_f32 v[22:23], v[12:13], v[22:23], v[86:87] op_sel_hi:[0,1,1]
	v_pk_fma_f32 v[20:21], v[12:13], v[20:21], v[94:95] op_sel_hi:[0,1,1]
	s_waitcnt lgkmcnt(3)
	v_pk_fma_f32 v[22:23], v[10:11], v[26:27], v[22:23] op_sel_hi:[0,1,1]
	ds_read_b128 v[26:29], v67 offset:43344
	ds_read_b128 v[60:63], v67 offset:43072
	ds_read_b128 v[44:47], v67 offset:43600
	ds_read_b128 v[74:77], v67 offset:43856
	ds_read_b128 v[78:81], v67 offset:43328
	s_waitcnt lgkmcnt(6)
	v_pk_fma_f32 v[22:23], v[6:7], v[40:41], v[22:23] op_sel_hi:[0,1,1]
	v_pk_fma_f32 v[20:21], v[10:11], v[24:25], v[20:21] op_sel_hi:[0,1,1]
	s_waitcnt lgkmcnt(4)
	v_pk_fma_f32 v[22:23], v[6:7], v[28:29], v[22:23] op_sel:[1,0,0]
	v_pk_fma_f32 v[24:25], v[6:7], v[38:39], v[20:21] op_sel_hi:[0,1,1]
	s_waitcnt lgkmcnt(2)
	v_pk_fma_f32 v[22:23], v[8:9], v[46:47], v[22:23] op_sel_hi:[0,1,1]
	s_waitcnt lgkmcnt(1)
	v_pk_fma_f32 v[28:29], v[50:51], v[76:77], v[22:23] op_sel_hi:[0,1,1]
	ds_read_b128 v[20:23], v67 offset:44112
	v_pk_fma_f32 v[24:25], v[6:7], v[26:27], v[24:25] op_sel:[1,0,0]
	ds_read_b128 v[82:85], v67 offset:43584
	ds_read_b128 v[86:89], v67 offset:43840
	v_pk_fma_f32 v[24:25], v[8:9], v[44:45], v[24:25] op_sel_hi:[0,1,1]
	v_pk_fma_f32 v[38:39], v[50:51], v[74:75], v[24:25] op_sel_hi:[0,1,1]
	ds_read_b128 v[24:27], v67 offset:44096
	s_waitcnt lgkmcnt(3)
	v_pk_fma_f32 v[106:107], v[2:3], v[20:21], v[38:39] op_sel_hi:[0,1,1]
	v_pk_fma_f32 v[20:21], v[12:13], v[54:55], v[92:93] op_sel_hi:[0,1,1]
	v_pk_fma_f32 v[20:21], v[10:11], v[58:59], v[20:21] op_sel_hi:[0,1,1]
	v_pk_fma_f32 v[20:21], v[6:7], v[62:63], v[20:21] op_sel_hi:[0,1,1]
	v_pk_fma_f32 v[108:109], v[2:3], v[22:23], v[28:29] op_sel_hi:[0,1,1]
	v_pk_fma_f32 v[28:29], v[6:7], v[80:81], v[20:21] op_sel:[1,0,0]
	ds_read_b128 v[20:23], v67 offset:44128
	s_waitcnt lgkmcnt(3)
	v_pk_fma_f32 v[28:29], v[8:9], v[84:85], v[28:29] op_sel_hi:[0,1,1]
	s_waitcnt lgkmcnt(2)
	v_pk_fma_f32 v[28:29], v[50:51], v[88:89], v[28:29] op_sel_hi:[0,1,1]
	ds_read_b128 v[38:41], v67 offset:44144
	s_waitcnt lgkmcnt(2)
	v_pk_fma_f32 v[110:111], v[2:3], v[26:27], v[28:29] op_sel_hi:[0,1,1]
	s_waitcnt lgkmcnt(1)
	v_pk_fma_f32 v[46:47], v[2:3], v[20:21], v[96:97] op_sel_hi:[0,1,1]
	v_pk_fma_f32 v[20:21], v[12:13], v[52:53], v[90:91] op_sel_hi:[0,1,1]
	v_pk_fma_f32 v[20:21], v[10:11], v[56:57], v[20:21] op_sel_hi:[0,1,1]
	v_pk_fma_f32 v[20:21], v[6:7], v[60:61], v[20:21] op_sel_hi:[0,1,1]
	v_pk_fma_f32 v[20:21], v[6:7], v[78:79], v[20:21] op_sel:[1,0,0]
	v_pk_fma_f32 v[44:45], v[2:3], v[22:23], v[64:65] op_sel_hi:[0,1,1]
	v_pk_fma_f32 v[26:27], v[8:9], v[82:83], v[20:21] op_sel_hi:[0,1,1]
	ds_read_b128 v[20:23], v67 offset:42544
	v_pk_fma_f32 v[26:27], v[50:51], v[86:87], v[26:27] op_sel_hi:[0,1,1]
	v_pk_fma_f32 v[64:65], v[2:3], v[24:25], v[26:27] op_sel_hi:[0,1,1]
	ds_read_b128 v[26:29], v67 offset:42800
	ds_read_b128 v[74:77], v67 offset:42528
	ds_read_b128 v[52:55], v67 offset:43056
	ds_read_b128 v[78:81], v67 offset:42784
	ds_read_b128 v[56:59], v67 offset:43312
	ds_read_b128 v[82:85], v67 offset:43040
	s_waitcnt lgkmcnt(6)
	v_pk_fma_f32 v[18:19], v[12:13], v[22:23], v[18:19] op_sel_hi:[0,1,1]
	ds_read_b128 v[60:63], v67 offset:43568
	ds_read_b128 v[86:89], v67 offset:43296
	s_waitcnt lgkmcnt(7)
	v_pk_fma_f32 v[18:19], v[10:11], v[28:29], v[18:19] op_sel_hi:[0,1,1]
	v_pk_fma_f32 v[38:39], v[2:3], v[38:39], v[98:99] op_sel_hi:[0,1,1]
	v_pk_fma_f32 v[40:41], v[2:3], v[40:41], v[100:101] op_sel_hi:[0,1,1]
	s_waitcnt lgkmcnt(5)
	v_pk_fma_f32 v[18:19], v[6:7], v[54:55], v[18:19] op_sel_hi:[0,1,1]
	ds_read_b128 v[90:93], v67 offset:43824
	ds_read_b128 v[94:97], v67 offset:44080
	ds_read_b128 v[98:101], v67 offset:43552
	v_pk_fma_f32 v[16:17], v[12:13], v[20:21], v[16:17] op_sel_hi:[0,1,1]
	s_waitcnt lgkmcnt(6)
	v_pk_fma_f32 v[18:19], v[6:7], v[58:59], v[18:19] op_sel:[1,0,0]
	v_pk_fma_f32 v[16:17], v[10:11], v[26:27], v[16:17] op_sel_hi:[0,1,1]
	s_waitcnt lgkmcnt(4)
	v_pk_fma_f32 v[18:19], v[8:9], v[62:63], v[18:19] op_sel_hi:[0,1,1]
	v_pk_fma_f32 v[16:17], v[6:7], v[52:53], v[16:17] op_sel_hi:[0,1,1]
	s_waitcnt lgkmcnt(2)
	v_pk_fma_f32 v[18:19], v[50:51], v[92:93], v[18:19] op_sel_hi:[0,1,1]
	v_pk_fma_f32 v[16:17], v[6:7], v[56:57], v[16:17] op_sel:[1,0,0]
	s_waitcnt lgkmcnt(1)
	v_pk_fma_f32 v[62:63], v[2:3], v[96:97], v[18:19] op_sel_hi:[0,1,1]
	v_pk_fma_f32 v[20:21], v[8:9], v[60:61], v[16:17] op_sel_hi:[0,1,1]
	ds_read_b128 v[16:19], v67 offset:44336
	ds_read_b128 v[102:105], v67 offset:43808
	ds_read_b128 v[22:25], v67 offset:44064
	v_pk_fma_f32 v[14:15], v[12:13], v[76:77], v[14:15] op_sel_hi:[0,1,1]
	v_pk_fma_f32 v[14:15], v[10:11], v[80:81], v[14:15] op_sel_hi:[0,1,1]
	v_pk_fma_f32 v[20:21], v[50:51], v[90:91], v[20:21] op_sel_hi:[0,1,1]
	ds_read_b128 v[52:55], v67 offset:44352
	ds_read_b128 v[26:29], v67 offset:44320
	v_pk_fma_f32 v[14:15], v[6:7], v[84:85], v[14:15] op_sel_hi:[0,1,1]
	v_pk_fma_f32 v[20:21], v[2:3], v[94:95], v[20:21] op_sel_hi:[0,1,1]
	v_pk_fma_f32 v[14:15], v[6:7], v[88:89], v[14:15] op_sel:[1,0,0]
	s_waitcnt lgkmcnt(4)
	v_pk_fma_f32 v[58:59], v[2:3], v[16:17], v[20:21] op_sel:[1,0,0]
	v_pk_fma_f32 v[60:61], v[2:3], v[18:19], v[62:63] op_sel:[1,0,0]
	ds_read_b128 v[16:19], v67 offset:44368
	v_pk_fma_f32 v[14:15], v[8:9], v[100:101], v[14:15] op_sel_hi:[0,1,1]
	s_waitcnt lgkmcnt(4)
	v_pk_fma_f32 v[14:15], v[50:51], v[104:105], v[14:15] op_sel_hi:[0,1,1]
	s_waitcnt lgkmcnt(3)
	v_pk_fma_f32 v[14:15], v[2:3], v[24:25], v[14:15] op_sel_hi:[0,1,1]
	s_waitcnt lgkmcnt(1)
	v_pk_fma_f32 v[62:63], v[2:3], v[28:29], v[14:15] op_sel:[1,0,0]
	v_pk_fma_f32 v[28:29], v[12:13], v[74:75], v[30:31] op_sel_hi:[0,1,1]
	v_pk_fma_f32 v[28:29], v[10:11], v[78:79], v[28:29] op_sel_hi:[0,1,1]
	v_lshlrev_b32_e32 v11, 3, v1
	s_waitcnt lgkmcnt(0)
	v_pk_fma_f32 v[56:57], v[2:3], v[16:17], v[106:107] op_sel:[1,0,0]
	v_pk_fma_f32 v[24:25], v[2:3], v[18:19], v[108:109] op_sel:[1,0,0]
	ds_read_b128 v[18:21], v67 offset:44384
	ds_read_b128 v[14:17], v67 offset:44400
	global_load_dwordx2 a[0:1], v11, s[6:7]
	v_pk_fma_f32 v[28:29], v[6:7], v[82:83], v[28:29] op_sel_hi:[0,1,1]
	v_pk_fma_f32 v[28:29], v[6:7], v[86:87], v[28:29] op_sel:[1,0,0]
	v_pk_fma_f32 v[52:53], v[2:3], v[52:53], v[64:65] op_sel:[1,0,0]
	v_pk_fma_f32 v[28:29], v[8:9], v[98:99], v[28:29] op_sel_hi:[0,1,1]
	v_pk_fma_f32 v[64:65], v[50:51], v[102:103], v[28:29] op_sel_hi:[0,1,1]
	ds_read_b128 v[28:31], v67 offset:42512
	ds_read_b128 v[74:77], v67 offset:42768
	ds_read_b128 v[78:81], v67 offset:42496
	ds_read_b128 v[82:85], v67 offset:43024
	ds_read_b128 v[86:89], v67 offset:42752
	v_pk_fma_f32 v[22:23], v[2:3], v[22:23], v[64:65] op_sel_hi:[0,1,1]
	ds_read_b128 v[90:93], v67 offset:43280
	ds_read_b128 v[94:97], v67 offset:43008
	v_pk_fma_f32 v[22:23], v[2:3], v[26:27], v[22:23] op_sel:[1,0,0]
	s_waitcnt lgkmcnt(6)
	v_pk_fma_f32 v[26:27], v[12:13], v[30:31], v[48:49] op_sel_hi:[0,1,1]
	ds_read_b128 v[98:101], v67 offset:43536
	ds_read_b128 v[102:105], v67 offset:43264
	v_pk_fma_f32 v[54:55], v[2:3], v[54:55], v[110:111] op_sel:[1,0,0]
	s_waitcnt lgkmcnt(7)
	v_pk_fma_f32 v[26:27], v[10:11], v[76:77], v[26:27] op_sel_hi:[0,1,1]
	ds_read_b128 v[106:109], v67 offset:43792
	ds_read_b128 v[110:113], v67 offset:43520
	s_waitcnt lgkmcnt(7)
	v_pk_fma_f32 v[26:27], v[6:7], v[84:85], v[26:27] op_sel_hi:[0,1,1]
	ds_read_b128 v[114:117], v67 offset:44048
	ds_read_b128 v[118:121], v67 offset:43776
	s_waitcnt lgkmcnt(7)
	v_pk_fma_f32 v[26:27], v[6:7], v[92:93], v[26:27] op_sel:[1,0,0]
	ds_read_b128 v[122:125], v67 offset:44304
	ds_read_b128 v[126:129], v67 offset:44032
	s_waitcnt lgkmcnt(7)
	v_pk_fma_f32 v[26:27], v[8:9], v[100:101], v[26:27] op_sel_hi:[0,1,1]
	s_waitcnt lgkmcnt(5)
	v_pk_fma_f32 v[26:27], v[50:51], v[108:109], v[26:27] op_sel_hi:[0,1,1]
	ds_read_b128 v[130:133], v67 offset:44560
	ds_read_b128 v[134:137], v67 offset:44576
	ds_read_b128 v[138:141], v67 offset:44288
	s_waitcnt lgkmcnt(6)
	v_pk_fma_f32 v[26:27], v[2:3], v[116:117], v[26:27] op_sel_hi:[0,1,1]
	s_waitcnt lgkmcnt(4)
	v_pk_fma_f32 v[26:27], v[2:3], v[124:125], v[26:27] op_sel:[1,0,0]
	ds_read_b128 v[142:145], v67 offset:44592
	ds_read_b128 v[146:149], v67 offset:44544
	s_waitcnt lgkmcnt(4)
	v_pk_fma_f32 v[30:31], v[4:5], v[132:133], v[26:27] op_sel_hi:[0,1,1]
	v_pk_fma_f32 v[26:27], v[12:13], v[28:29], v[42:43] op_sel_hi:[0,1,1]
	v_pk_fma_f32 v[26:27], v[10:11], v[74:75], v[26:27] op_sel_hi:[0,1,1]
	v_pk_fma_f32 v[26:27], v[6:7], v[82:83], v[26:27] op_sel_hi:[0,1,1]
	v_pk_fma_f32 v[26:27], v[6:7], v[90:91], v[26:27] op_sel:[1,0,0]
	s_waitcnt lgkmcnt(1)
	v_pk_fma_f32 v[76:77], v[4:5], v[142:143], v[58:59] op_sel_hi:[0,1,1]
	v_pk_fma_f32 v[26:27], v[8:9], v[98:99], v[26:27] op_sel_hi:[0,1,1]
	v_pk_fma_f32 v[26:27], v[50:51], v[106:107], v[26:27] op_sel_hi:[0,1,1]
	v_pk_fma_f32 v[26:27], v[2:3], v[114:115], v[26:27] op_sel_hi:[0,1,1]
	v_pk_fma_f32 v[26:27], v[2:3], v[122:123], v[26:27] op_sel:[1,0,0]
	v_pk_fma_f32 v[84:85], v[4:5], v[144:145], v[60:61] op_sel_hi:[0,1,1]
	v_pk_fma_f32 v[42:43], v[4:5], v[130:131], v[26:27] op_sel_hi:[0,1,1]
	v_pk_fma_f32 v[26:27], v[12:13], v[80:81], v[36:37] op_sel_hi:[0,1,1]
	v_pk_fma_f32 v[12:13], v[12:13], v[78:79], v[34:35] op_sel_hi:[0,1,1]
	v_pk_fma_f32 v[26:27], v[10:11], v[88:89], v[26:27] op_sel_hi:[0,1,1]
	v_pk_fma_f32 v[10:11], v[10:11], v[86:87], v[12:13] op_sel_hi:[0,1,1]
	v_pk_fma_f32 v[26:27], v[6:7], v[96:97], v[26:27] op_sel_hi:[0,1,1]
	v_pk_fma_f32 v[10:11], v[6:7], v[94:95], v[10:11] op_sel_hi:[0,1,1]
	v_pk_fma_f32 v[26:27], v[6:7], v[104:105], v[26:27] op_sel:[1,0,0]
	v_pk_fma_f32 v[6:7], v[6:7], v[102:103], v[10:11] op_sel:[1,0,0]
	v_pk_fma_f32 v[26:27], v[8:9], v[112:113], v[26:27] op_sel_hi:[0,1,1]
	v_pk_fma_f32 v[6:7], v[8:9], v[110:111], v[6:7] op_sel_hi:[0,1,1]
	v_pk_fma_f32 v[26:27], v[50:51], v[120:121], v[26:27] op_sel_hi:[0,1,1]
	v_pk_fma_f32 v[6:7], v[50:51], v[118:119], v[6:7] op_sel_hi:[0,1,1]
	v_pk_fma_f32 v[36:37], v[2:3], v[128:129], v[26:27] op_sel_hi:[0,1,1]
	ds_read_b128 v[26:29], v67 offset:44800
	ds_read_b128 v[58:61], v67 offset:44816
	v_pk_fma_f32 v[10:11], v[2:3], v[126:127], v[6:7] op_sel_hi:[0,1,1]
	ds_read_b128 v[6:9], v67 offset:45056
	v_pk_fma_f32 v[34:35], v[2:3], v[138:139], v[10:11] op_sel:[1,0,0]
	ds_read_b128 v[10:13], v67 offset:45072
	v_pk_fma_f32 v[36:37], v[2:3], v[140:141], v[36:37] op_sel:[1,0,0]
	v_mov_b32_e32 v32, v5
	s_waitcnt lgkmcnt(4)
	v_pk_fma_f32 v[36:37], v[4:5], v[148:149], v[36:37] op_sel_hi:[0,1,1]
	v_pk_fma_f32 v[34:35], v[4:5], v[146:147], v[34:35] op_sel_hi:[0,1,1]
	s_waitcnt lgkmcnt(3)
	v_pk_fma_f32 v[36:37], v[32:33], v[28:29], v[36:37] op_sel_hi:[0,1,1]
	s_waitcnt lgkmcnt(2)
	v_pk_fma_f32 v[42:43], v[32:33], v[58:59], v[42:43] op_sel_hi:[0,1,1]
	v_pk_fma_f32 v[58:59], v[32:33], v[60:61], v[30:31] op_sel_hi:[0,1,1]
	v_pk_fma_f32 v[26:27], v[32:33], v[26:27], v[34:35] op_sel_hi:[0,1,1]
	s_waitcnt lgkmcnt(1)
	v_pk_fma_f32 v[6:7], v[68:69], v[6:7], v[26:27] op_sel_hi:[0,1,1]
	v_pk_fma_f32 v[8:9], v[68:69], v[8:9], v[36:37] op_sel_hi:[0,1,1]
	s_waitcnt lgkmcnt(0)
	v_pk_fma_f32 v[10:11], v[68:69], v[10:11], v[42:43] op_sel_hi:[0,1,1]
	v_pk_fma_f32 v[12:13], v[68:69], v[12:13], v[58:59] op_sel_hi:[0,1,1]
	v_lshlrev_b32_e32 v33, 4, v72
	v_pk_fma_f32 v[48:49], v[4:5], v[136:137], v[62:63] op_sel_hi:[0,1,1]
	ds_read_b128 v[62:65], v67 offset:44832
	v_cvt_pk_f16_f32 v6, v6, v7
	v_cvt_pk_f16_f32 v7, v8, v9
	v_cvt_pk_f16_f32 v8, v10, v11
	v_cvt_pk_f16_f32 v9, v12, v13
	ds_read_b128 v[10:13], v33
	ds_read_b128 v[28:31], v67 offset:44848
	v_pk_fma_f32 v[22:23], v[4:5], v[134:135], v[22:23] op_sel_hi:[0,1,1]
	s_waitcnt lgkmcnt(2)
	v_pk_fma_f32 v[22:23], v[32:33], v[62:63], v[22:23] op_sel_hi:[0,1,1]
	s_waitcnt vmcnt(0)
	v_accvgpr_mov_b32 a16, a0
	v_accvgpr_mov_b32 a17, a0
	v_accvgpr_mov_b32 a18, a0
	v_accvgpr_mov_b32 a19, a0
	v_accvgpr_mov_b32 a20, a0
	v_accvgpr_mov_b32 a21, a0
	v_accvgpr_mov_b32 a22, a0
	v_accvgpr_mov_b32 a23, a0
	v_accvgpr_mov_b32 a24, a0
	v_accvgpr_mov_b32 a25, a0
	v_accvgpr_mov_b32 a26, a0
	v_accvgpr_mov_b32 a27, a0
	v_accvgpr_mov_b32 a28, a0
	v_accvgpr_mov_b32 a29, a0
	v_accvgpr_mov_b32 a30, a0
	v_accvgpr_mov_b32 a31, a0
	v_accvgpr_mov_b32 a0, a1
	v_accvgpr_mov_b32 a2, a1
	s_waitcnt lgkmcnt(1)
	v_mfma_f32_32x32x16_f16 a[16:31], v[6:9], v[10:13], a[16:31]
	ds_read_b128 v[10:13], v33 offset:4096
	v_accvgpr_mov_b32 a3, a1
	v_accvgpr_mov_b32 a4, a1
	v_accvgpr_mov_b32 a5, a1
	v_accvgpr_mov_b32 a6, a1
	v_accvgpr_mov_b32 a7, a1
	v_accvgpr_mov_b32 a8, a1
	v_accvgpr_mov_b32 a9, a1
	v_accvgpr_mov_b32 a10, a1
	v_accvgpr_mov_b32 a11, a1
	v_accvgpr_mov_b32 a12, a1
	v_accvgpr_mov_b32 a13, a1
	v_accvgpr_mov_b32 a14, a1
	v_accvgpr_mov_b32 a15, a1
	v_pk_fma_f32 v[42:43], v[32:33], v[64:65], v[48:49] op_sel_hi:[0,1,1]
	s_waitcnt lgkmcnt(1)
	v_pk_fma_f32 v[62:63], v[32:33], v[28:29], v[76:77] op_sel_hi:[0,1,1]
	s_waitcnt lgkmcnt(0)
	v_mfma_f32_32x32x16_f16 a[0:15], v[6:9], v[10:13], a[0:15]
	ds_read_b128 v[34:37], v33 offset:1024
	ds_read_b128 v[10:13], v33 offset:8192
	ds_read_b128 v[48:51], v67 offset:45088
	ds_read_b128 v[58:61], v33 offset:12288
	ds_read_b128 v[26:29], v67 offset:45104
	v_pk_fma_f32 v[38:39], v[2:3], v[14:15], v[38:39] op_sel:[1,0,0]
	s_load_dwordx4 s[4:7], s[0:1], 0x40
	v_lshlrev_b32_e32 v1, 2, v1
	s_waitcnt lgkmcnt(0)
	v_mfma_f32_32x32x16_f16 a[16:31], v[6:9], v[10:13], a[16:31]
	v_fma_f32 v10, v32, v30, v84
	v_fma_f32 v11, v32, v31, v85
	v_fma_f32 v12, v68, v48, v22
	v_fma_f32 v13, v68, v49, v23
	v_fma_f32 v22, v68, v50, v42
	v_fma_f32 v23, v68, v51, v43
	v_pk_fma_f32 v[26:27], v[68:69], v[26:27], v[62:63] op_sel_hi:[0,1,1]
	v_pk_fma_f32 v[28:29], v[68:69], v[28:29], v[10:11] op_sel_hi:[0,1,1]
	v_cvt_pk_f16_f32 v10, v12, v13
	v_cvt_pk_f16_f32 v11, v22, v23
	v_cvt_pk_f16_f32 v12, v26, v27
	v_cvt_pk_f16_f32 v13, v28, v29
	v_mfma_f32_32x32x16_f16 a[0:15], v[6:9], v[58:61], a[0:15]
	ds_read_b128 v[26:29], v33 offset:5120
	ds_read_b128 v[48:51], v33 offset:9216
	ds_read_b128 v[58:61], v33 offset:13312
	ds_read_b128 v[62:65], v67 offset:44608
	v_fma_f32 v30, v3, v18, v46
	v_fma_f32 v31, v3, v19, v47
	v_pk_fma_f32 v[42:43], v[2:3], v[20:21], v[44:45] op_sel:[1,0,0]
	ds_read_b128 v[18:21], v67 offset:44864
	v_pk_fma_f32 v[2:3], v[2:3], v[16:17], v[40:41] op_sel:[1,0,0]
	s_waitcnt lgkmcnt(1)
	v_pk_fma_f32 v[22:23], v[4:5], v[62:63], v[52:53] op_sel_hi:[0,1,1]
	v_pk_fma_f32 v[44:45], v[4:5], v[64:65], v[54:55] op_sel_hi:[0,1,1]
	v_mfma_f32_32x32x16_f16 a[16:31], v[10:13], v[34:37], a[16:31]
	ds_read_b128 v[34:37], v67 offset:44624
	s_waitcnt lgkmcnt(1)
	v_fma_f32 v46, v32, v18, v22
	v_fma_f32 v47, v32, v19, v23
	v_fma_f32 v44, v32, v20, v44
	v_fma_f32 v45, v32, v21, v45
	ds_read_b128 v[18:21], v67 offset:45120
	s_waitcnt lgkmcnt(1)
	v_pk_fma_f32 v[36:37], v[4:5], v[36:37], v[24:25] op_sel_hi:[0,1,1]
	ds_read_b128 v[22:25], v67 offset:45136
	v_mfma_f32_32x32x16_f16 a[0:15], v[10:13], v[26:29], a[0:15]
	ds_read_b128 v[26:29], v67 offset:44880
	v_fma_f32 v34, v4, v34, v56
	v_fma_f32 v35, v4, v35, v57
	s_waitcnt lgkmcnt(2)
	v_fma_f32 v18, v68, v18, v46
	v_fma_f32 v19, v68, v19, v47
	v_pk_fma_f32 v[20:21], v[68:69], v[20:21], v[44:45] op_sel_hi:[0,1,1]
	v_cvt_pk_f16_f32 v18, v18, v19
	s_waitcnt lgkmcnt(0)
	v_pk_fma_f32 v[26:27], v[32:33], v[26:27], v[34:35] op_sel_hi:[0,1,1]
	v_pk_fma_f32 v[28:29], v[32:33], v[28:29], v[36:37] op_sel_hi:[0,1,1]
	v_mfma_f32_32x32x16_f16 a[16:31], v[10:13], v[48:51], a[16:31]
	v_fma_f32 v22, v68, v22, v26
	v_fma_f32 v23, v68, v23, v27
	v_fma_f32 v24, v68, v24, v28
	v_fma_f32 v25, v68, v25, v29
	v_cvt_pk_f16_f32 v19, v20, v21
	v_cvt_pk_f16_f32 v20, v22, v23
	v_cvt_pk_f16_f32 v21, v24, v25
	ds_read_b128 v[22:25], v33 offset:2048
	ds_read_b128 v[26:29], v67 offset:44640
	ds_read_b128 v[14:17], v67 offset:44656
	v_mfma_f32_32x32x16_f16 a[0:15], v[10:13], v[58:61], a[0:15]
	s_waitcnt lgkmcnt(1)
	v_fma_f32 v30, v4, v26, v30
	v_fma_f32 v31, v4, v27, v31
	v_fma_f32 v40, v4, v28, v42
	v_fma_f32 v41, v4, v29, v43
	s_waitcnt lgkmcnt(0)
	v_pk_fma_f32 v[38:39], v[4:5], v[14:15], v[38:39] op_sel_hi:[0,1,1]
	v_pk_fma_f32 v[42:43], v[4:5], v[16:17], v[2:3] op_sel_hi:[0,1,1]
	v_mfma_f32_32x32x16_f16 a[16:31], v[18:21], v[22:25], a[16:31]
	ds_read_b128 v[22:25], v33 offset:6144
	ds_read_b128 v[26:29], v33 offset:3072
	ds_read_b128 v[34:37], v67 offset:44896
	ds_read_b128 v[2:5], v67 offset:44912
	ds_read_b128 v[14:17], v33 offset:10240
	s_waitcnt lgkmcnt(2)
	v_pk_fma_f32 v[30:31], v[32:33], v[34:35], v[30:31] op_sel_hi:[0,1,1]
	v_pk_fma_f32 v[40:41], v[32:33], v[36:37], v[40:41] op_sel_hi:[0,1,1]
	v_mfma_f32_32x32x16_f16 a[0:15], v[18:21], v[22:25], a[0:15]
	ds_read_b128 v[22:25], v67 offset:45152
	ds_read_b128 v[34:37], v67 offset:45168
	s_waitcnt lgkmcnt(3)
	v_fma_f32 v38, v32, v2, v38
	v_fma_f32 v39, v32, v3, v39
	s_waitcnt lgkmcnt(2)
	v_mfma_f32_32x32x16_f16 a[16:31], v[18:21], v[14:17], a[16:31]
	v_fma_f32 v14, v32, v4, v42
	v_fma_f32 v15, v32, v5, v43
	ds_read_b128 v[2:5], v33 offset:14336
	s_waitcnt lgkmcnt(2)
	v_fma_f32 v16, v68, v22, v30
	v_fma_f32 v17, v68, v23, v31
	v_pk_fma_f32 v[22:23], v[68:69], v[24:25], v[40:41] op_sel_hi:[0,1,1]
	s_waitcnt lgkmcnt(1)
	v_pk_fma_f32 v[24:25], v[68:69], v[34:35], v[38:39] op_sel_hi:[0,1,1]
	v_pk_fma_f32 v[30:31], v[68:69], v[36:37], v[14:15] op_sel_hi:[0,1,1]
	v_cvt_pk_f16_f32 v14, v16, v17
	s_waitcnt lgkmcnt(0)
	v_mfma_f32_32x32x16_f16 a[0:15], v[18:21], v[2:5], a[0:15]
	v_cvt_pk_f16_f32 v15, v22, v23
	v_cvt_pk_f16_f32 v16, v24, v25
	v_cvt_pk_f16_f32 v17, v30, v31
	ds_read_b128 v[2:5], v33 offset:7168
	ds_read_b128 v[22:25], v33 offset:31744
	v_ashrrev_i32_e32 v67, 31, v66
	v_mfma_f32_32x32x16_f16 a[16:31], v[14:17], v[26:29], a[16:31]
	v_lshlrev_b64 v[26:27], 7, v[66:67]
	v_lshl_add_u64 v[26:27], s[4:5], 0, v[26:27]
	s_waitcnt lgkmcnt(1)
	v_mfma_f32_32x32x16_f16 a[0:15], v[14:17], v[2:5], a[0:15]
	ds_read_b128 v[2:5], v33 offset:11264
	s_waitcnt lgkmcnt(0)
	v_mfma_f32_32x32x16_f16 a[16:31], v[14:17], v[2:5], a[16:31]
	ds_read_b128 v[2:5], v33 offset:15360
	s_waitcnt lgkmcnt(0)
	v_mfma_f32_32x32x16_f16 a[0:15], v[14:17], v[2:5], a[0:15]
	ds_read_b128 v[2:5], v33 offset:16384
	s_waitcnt lgkmcnt(0)
	v_mfma_f32_32x32x16_f16 a[32:47], v[6:9], v[2:5], 0
	ds_read_b128 v[2:5], v33 offset:20480
	s_waitcnt lgkmcnt(0)
	v_mfma_f32_32x32x16_f16 a[48:63], v[6:9], v[2:5], 0
	ds_read_b128 v[2:5], v33 offset:24576
	s_waitcnt lgkmcnt(0)
	v_mfma_f32_32x32x16_f16 a[32:47], v[6:9], v[2:5], a[32:47]
	ds_read_b128 v[2:5], v33 offset:28672
	s_waitcnt lgkmcnt(0)
	v_mfma_f32_32x32x16_f16 a[48:63], v[6:9], v[2:5], a[48:63]
	ds_read_b128 v[2:5], v33 offset:17408
	s_waitcnt lgkmcnt(0)
	v_mfma_f32_32x32x16_f16 a[32:47], v[10:13], v[2:5], a[32:47]
	ds_read_b128 v[2:5], v33 offset:21504
	s_waitcnt lgkmcnt(0)
	v_mfma_f32_32x32x16_f16 a[48:63], v[10:13], v[2:5], a[48:63]
	ds_read_b128 v[2:5], v33 offset:25600
	s_waitcnt lgkmcnt(0)
	v_mfma_f32_32x32x16_f16 a[32:47], v[10:13], v[2:5], a[32:47]
	ds_read_b128 v[2:5], v33 offset:29696
	s_waitcnt lgkmcnt(0)
	v_mfma_f32_32x32x16_f16 a[48:63], v[10:13], v[2:5], a[48:63]
	ds_read_b128 v[2:5], v33 offset:18432
	s_waitcnt lgkmcnt(0)
	v_mfma_f32_32x32x16_f16 a[32:47], v[18:21], v[2:5], a[32:47]
	ds_read_b128 v[2:5], v33 offset:22528
	s_waitcnt lgkmcnt(0)
	v_mfma_f32_32x32x16_f16 a[48:63], v[18:21], v[2:5], a[48:63]
	ds_read_b128 v[2:5], v33 offset:26624
	s_waitcnt lgkmcnt(0)
	v_mfma_f32_32x32x16_f16 a[32:47], v[18:21], v[2:5], a[32:47]
	ds_read_b128 v[2:5], v33 offset:30720
	s_waitcnt lgkmcnt(0)
	v_mfma_f32_32x32x16_f16 a[48:63], v[18:21], v[2:5], a[48:63]
	ds_read_b128 v[2:5], v33 offset:19456
	s_waitcnt lgkmcnt(0)
	v_mfma_f32_32x32x16_f16 a[32:47], v[14:17], v[2:5], a[32:47]
	ds_read_b128 v[2:5], v33 offset:23552
	s_waitcnt lgkmcnt(0)
	v_mfma_f32_32x32x16_f16 a[48:63], v[14:17], v[2:5], a[48:63]
	ds_read_b128 v[2:5], v33 offset:27648
	s_waitcnt lgkmcnt(0)
	v_mfma_f32_32x32x16_f16 a[32:47], v[14:17], v[2:5], a[32:47]
	v_lshlrev_b32_e32 v2, 1, v71
	v_mov_b32_e32 v3, 0
	v_lshl_add_u64 v[2:3], v[26:27], 0, v[2:3]
	global_store_dwordx4 v[2:3], v[6:9], off
	global_store_dwordx4 v[2:3], v[10:13], off offset:16
	global_store_dwordx4 v[2:3], v[18:21], off offset:32
	global_store_dwordx4 v[2:3], v[14:17], off offset:48
	v_lshrrev_b32_e32 v2, 3, v0
	v_and_or_b32 v2, v2, 4, v69
	v_ashrrev_i32_e32 v3, 31, v2
	v_mfma_f32_32x32x16_f16 a[48:63], v[14:17], v[22:25], a[48:63]
	v_accvgpr_read_b32 v4, a0
	v_accvgpr_read_b32 v5, a16
	v_cvt_pk_bf16_f32 v8, v5, v4
	v_lshlrev_b64 v[4:5], 7, v[2:3]
	v_or_b32_e32 v4, v4, v1
	v_lshl_add_u64 v[6:7], s[6:7], 0, v[4:5]
	global_store_dword v[6:7], v8, off
	v_accvgpr_read_b32 v6, a32
	v_lshl_add_u64 v[4:5], s[10:11], 0, v[4:5]
	s_nop 2
	v_accvgpr_read_b32 v3, a48
	v_cvt_pk_bf16_f32 v3, v6, v3
	global_store_dword v[4:5], v3, off
	v_or_b32_e32 v4, 1, v2
	v_ashrrev_i32_e32 v5, 31, v4
	v_lshlrev_b64 v[4:5], 7, v[4:5]
	v_accvgpr_read_b32 v3, a1
	v_accvgpr_read_b32 v6, a17
	v_or_b32_e32 v4, v4, v1
	v_cvt_pk_bf16_f32 v3, v6, v3
	v_lshl_add_u64 v[6:7], s[6:7], 0, v[4:5]
	global_store_dword v[6:7], v3, off
	v_accvgpr_read_b32 v3, a49
	v_accvgpr_read_b32 v6, a33
	v_cvt_pk_bf16_f32 v3, v6, v3
	v_lshl_add_u64 v[4:5], s[10:11], 0, v[4:5]
	global_store_dword v[4:5], v3, off
	v_or_b32_e32 v4, 2, v2
	v_ashrrev_i32_e32 v5, 31, v4
	v_lshlrev_b64 v[4:5], 7, v[4:5]
	v_accvgpr_read_b32 v3, a2
	v_accvgpr_read_b32 v6, a18
	v_or_b32_e32 v4, v4, v1
	v_cvt_pk_bf16_f32 v3, v6, v3
	v_lshl_add_u64 v[6:7], s[6:7], 0, v[4:5]
	global_store_dword v[6:7], v3, off
	v_accvgpr_read_b32 v3, a50
	v_accvgpr_read_b32 v6, a34
	v_cvt_pk_bf16_f32 v3, v6, v3
	v_lshl_add_u64 v[4:5], s[10:11], 0, v[4:5]
	global_store_dword v[4:5], v3, off
	v_or_b32_e32 v4, 3, v2
	v_ashrrev_i32_e32 v5, 31, v4
	v_lshlrev_b64 v[4:5], 7, v[4:5]
	v_accvgpr_read_b32 v3, a3
	v_accvgpr_read_b32 v6, a19
	v_or_b32_e32 v4, v4, v1
	v_cvt_pk_bf16_f32 v3, v6, v3
	v_lshl_add_u64 v[6:7], s[6:7], 0, v[4:5]
	global_store_dword v[6:7], v3, off
	v_accvgpr_read_b32 v3, a51
	v_accvgpr_read_b32 v6, a35
	v_cvt_pk_bf16_f32 v3, v6, v3
	v_lshl_add_u64 v[4:5], s[10:11], 0, v[4:5]
	global_store_dword v[4:5], v3, off
	v_or_b32_e32 v4, 8, v2
	v_ashrrev_i32_e32 v5, 31, v4
	v_lshlrev_b64 v[4:5], 7, v[4:5]
	v_accvgpr_read_b32 v3, a4
	v_accvgpr_read_b32 v6, a20
	v_or_b32_e32 v4, v4, v1
	v_cvt_pk_bf16_f32 v3, v6, v3
	v_lshl_add_u64 v[6:7], s[6:7], 0, v[4:5]
	global_store_dword v[6:7], v3, off
	v_accvgpr_read_b32 v3, a52
	v_accvgpr_read_b32 v6, a36
	v_cvt_pk_bf16_f32 v3, v6, v3
	v_lshl_add_u64 v[4:5], s[10:11], 0, v[4:5]
	global_store_dword v[4:5], v3, off
	v_or_b32_e32 v4, 9, v2
	v_ashrrev_i32_e32 v5, 31, v4
	v_lshlrev_b64 v[4:5], 7, v[4:5]
	v_accvgpr_read_b32 v3, a5
	v_accvgpr_read_b32 v6, a21
	v_or_b32_e32 v4, v4, v1
	v_cvt_pk_bf16_f32 v3, v6, v3
	v_lshl_add_u64 v[6:7], s[6:7], 0, v[4:5]
	global_store_dword v[6:7], v3, off
	v_accvgpr_read_b32 v3, a53
	v_accvgpr_read_b32 v6, a37
	v_cvt_pk_bf16_f32 v3, v6, v3
	v_lshl_add_u64 v[4:5], s[10:11], 0, v[4:5]
	global_store_dword v[4:5], v3, off
	v_or_b32_e32 v4, 10, v2
	v_ashrrev_i32_e32 v5, 31, v4
	v_lshlrev_b64 v[4:5], 7, v[4:5]
	v_accvgpr_read_b32 v3, a6
	v_accvgpr_read_b32 v6, a22
	v_or_b32_e32 v4, v4, v1
	v_cvt_pk_bf16_f32 v3, v6, v3
	v_lshl_add_u64 v[6:7], s[6:7], 0, v[4:5]
	global_store_dword v[6:7], v3, off
	v_accvgpr_read_b32 v3, a54
	v_accvgpr_read_b32 v6, a38
	v_cvt_pk_bf16_f32 v3, v6, v3
	v_lshl_add_u64 v[4:5], s[10:11], 0, v[4:5]
	global_store_dword v[4:5], v3, off
	v_or_b32_e32 v4, 11, v2
	v_ashrrev_i32_e32 v5, 31, v4
	v_lshlrev_b64 v[4:5], 7, v[4:5]
	v_accvgpr_read_b32 v3, a7
	v_accvgpr_read_b32 v6, a23
	v_or_b32_e32 v4, v4, v1
	v_cvt_pk_bf16_f32 v3, v6, v3
	v_lshl_add_u64 v[6:7], s[6:7], 0, v[4:5]
	global_store_dword v[6:7], v3, off
	v_accvgpr_read_b32 v3, a55
	v_accvgpr_read_b32 v6, a39
	v_cvt_pk_bf16_f32 v3, v6, v3
	v_lshl_add_u64 v[4:5], s[10:11], 0, v[4:5]
	global_store_dword v[4:5], v3, off
	v_or_b32_e32 v4, 16, v2
	v_ashrrev_i32_e32 v5, 31, v4
	v_lshlrev_b64 v[4:5], 7, v[4:5]
	v_accvgpr_read_b32 v3, a8
	v_accvgpr_read_b32 v6, a24
	v_or_b32_e32 v4, v4, v1
	v_cvt_pk_bf16_f32 v3, v6, v3
	v_lshl_add_u64 v[6:7], s[6:7], 0, v[4:5]
	global_store_dword v[6:7], v3, off
	v_accvgpr_read_b32 v3, a56
	v_accvgpr_read_b32 v6, a40
	v_cvt_pk_bf16_f32 v3, v6, v3
	v_lshl_add_u64 v[4:5], s[10:11], 0, v[4:5]
	global_store_dword v[4:5], v3, off
	v_or_b32_e32 v4, 17, v2
	v_ashrrev_i32_e32 v5, 31, v4
	v_lshlrev_b64 v[4:5], 7, v[4:5]
	v_accvgpr_read_b32 v3, a9
	v_accvgpr_read_b32 v6, a25
	v_or_b32_e32 v4, v4, v1
	v_cvt_pk_bf16_f32 v3, v6, v3
	v_lshl_add_u64 v[6:7], s[6:7], 0, v[4:5]
	global_store_dword v[6:7], v3, off
	v_accvgpr_read_b32 v3, a57
	v_accvgpr_read_b32 v6, a41
	v_cvt_pk_bf16_f32 v3, v6, v3
	v_lshl_add_u64 v[4:5], s[10:11], 0, v[4:5]
	global_store_dword v[4:5], v3, off
	v_or_b32_e32 v4, 18, v2
	v_ashrrev_i32_e32 v5, 31, v4
	v_lshlrev_b64 v[4:5], 7, v[4:5]
	v_accvgpr_read_b32 v3, a10
	v_accvgpr_read_b32 v6, a26
	v_or_b32_e32 v4, v4, v1
	v_cvt_pk_bf16_f32 v3, v6, v3
	v_lshl_add_u64 v[6:7], s[6:7], 0, v[4:5]
	global_store_dword v[6:7], v3, off
	v_accvgpr_read_b32 v3, a58
	v_accvgpr_read_b32 v6, a42
	v_cvt_pk_bf16_f32 v3, v6, v3
	v_lshl_add_u64 v[4:5], s[10:11], 0, v[4:5]
	global_store_dword v[4:5], v3, off
	v_or_b32_e32 v4, 19, v2
	v_ashrrev_i32_e32 v5, 31, v4
	v_lshlrev_b64 v[4:5], 7, v[4:5]
	v_accvgpr_read_b32 v3, a11
	v_accvgpr_read_b32 v6, a27
	v_or_b32_e32 v4, v4, v1
	v_cvt_pk_bf16_f32 v3, v6, v3
	v_lshl_add_u64 v[6:7], s[6:7], 0, v[4:5]
	global_store_dword v[6:7], v3, off
	v_accvgpr_read_b32 v3, a59
	v_accvgpr_read_b32 v6, a43
	v_cvt_pk_bf16_f32 v3, v6, v3
	v_lshl_add_u64 v[4:5], s[10:11], 0, v[4:5]
	global_store_dword v[4:5], v3, off
	v_or_b32_e32 v4, 24, v2
	v_ashrrev_i32_e32 v5, 31, v4
	v_lshlrev_b64 v[4:5], 7, v[4:5]
	v_accvgpr_read_b32 v3, a12
	v_accvgpr_read_b32 v6, a28
	v_or_b32_e32 v4, v4, v1
	v_cvt_pk_bf16_f32 v3, v6, v3
	v_lshl_add_u64 v[6:7], s[6:7], 0, v[4:5]
	global_store_dword v[6:7], v3, off
	v_accvgpr_read_b32 v3, a60
	v_accvgpr_read_b32 v6, a44
	v_cvt_pk_bf16_f32 v3, v6, v3
	v_lshl_add_u64 v[4:5], s[10:11], 0, v[4:5]
	global_store_dword v[4:5], v3, off
	v_or_b32_e32 v4, 25, v2
	v_ashrrev_i32_e32 v5, 31, v4
	v_lshlrev_b64 v[4:5], 7, v[4:5]
	v_accvgpr_read_b32 v3, a13
	v_accvgpr_read_b32 v6, a29
	v_or_b32_e32 v4, v4, v1
	v_cvt_pk_bf16_f32 v3, v6, v3
	v_lshl_add_u64 v[6:7], s[6:7], 0, v[4:5]
	global_store_dword v[6:7], v3, off
	v_accvgpr_read_b32 v3, a61
	v_accvgpr_read_b32 v6, a45
	v_cvt_pk_bf16_f32 v3, v6, v3
	v_lshl_add_u64 v[4:5], s[10:11], 0, v[4:5]
	global_store_dword v[4:5], v3, off
	v_or_b32_e32 v4, 26, v2
	v_ashrrev_i32_e32 v5, 31, v4
	v_lshlrev_b64 v[4:5], 7, v[4:5]
	v_accvgpr_read_b32 v3, a14
	v_accvgpr_read_b32 v6, a30
	v_or_b32_e32 v4, v4, v1
	v_cvt_pk_bf16_f32 v3, v6, v3
	v_lshl_add_u64 v[6:7], s[6:7], 0, v[4:5]
	global_store_dword v[6:7], v3, off
	v_accvgpr_read_b32 v3, a62
	v_accvgpr_read_b32 v6, a46
	v_cvt_pk_bf16_f32 v3, v6, v3
	v_lshl_add_u64 v[4:5], s[10:11], 0, v[4:5]
	v_or_b32_e32 v2, 27, v2
	global_store_dword v[4:5], v3, off
	v_ashrrev_i32_e32 v3, 31, v2
	v_lshlrev_b64 v[2:3], 7, v[2:3]
	v_accvgpr_read_b32 v4, a15
	v_accvgpr_read_b32 v5, a31
	v_or_b32_e32 v2, v2, v1
	v_cvt_pk_bf16_f32 v6, v5, v4
	v_lshl_add_u64 v[4:5], s[6:7], 0, v[2:3]
	global_store_dword v[4:5], v6, off
	v_accvgpr_read_b32 v1, a63
	v_accvgpr_read_b32 v4, a47
	v_cvt_pk_bf16_f32 v1, v4, v1
	v_lshl_add_u64 v[2:3], s[10:11], 0, v[2:3]
	global_store_dword v[2:3], v1, off
